# speedup vs baseline: 1.0049x; 1.0049x over previous
_Z16closed_form_mainPKfS0_PKiPf:
	s_load_dwordx8 s[16:23], s[0:1], 0x0
	s_lshr_b32 s6, s2, 3
	v_readfirstlane_b32 s0, v0
	s_mul_hi_u32 s7, s6, 0x24924925
	s_lshr_b32 s4, s0, 6
	s_and_b32 s0, s2, 7
	s_mul_i32 s1, s7, 7
	s_bfe_u32 s5, s2, 0x10003
	s_sub_i32 s1, s6, s1
	s_mul_i32 s36, s0, 7
	s_xor_b32 s3, s4, s5
	s_add_i32 s36, s36, s1
	s_waitcnt lgkmcnt(0)
	s_mov_b64 s[28:29], s[22:23]
	v_and_b32_e32 v19, 63, v0
	s_cmp_lt_u32 s36, 52
	s_mov_b64 s[0:1], -1
	s_cbranch_scc0 .LBB0_32
	s_mul_hi_u32 s0, s6, 0x20820821
	s_lshr_b32 s38, s0, 3
	s_mul_hi_u32 s0, s7, 0x1c71c71d
	s_mul_i32 s0, s0, 9
	s_sub_i32 s0, s7, s0
	v_add_u32_e32 v2, -3, v19
	v_mad_u64_u32 v[0:1], s[0:1], s0, 57, v[2:3]
	s_mov_b64 s[24:25], s[18:19]
	v_mov_b32_e32 v1, 0x200
	v_med3_i32 v1, v0, 0, v1
	s_mul_i32 s34, s36, 10
	s_and_b32 s17, s17, 0xffff
	s_and_b32 s25, s25, 0xffff
	v_cmp_gt_u32_e64 s[0:1], 57, v2
	s_mov_b32 s19, 0x20000
	s_mov_b32 s18, 0xe0e038
	s_mov_b32 s26, 0x606018
	s_mul_i32 s35, s38, 0x70701c
	s_mul_i32 s33, s38, 0x30300c
	v_lshlrev_b32_e32 v28, 2, v1
	v_mul_u32_u24_e32 v27, 12, v1
	v_lshlrev_b32_e32 v23, 4, v19
	s_cmp_lg_u32 s4, s5
	v_sub_u32_e64 v29, s34, 2 clamp
	s_cbranch_scc0 .LBB0_15
	s_setprio 2
	s_mov_b32 s27, s19
	s_and_b32 s21, s21, 0xffff
	s_mov_b32 s22, 0x202008
	s_mov_b32 s23, s19
	s_mul_i32 s38, s38, 0x101004
	s_movk_i32 s37, 0x80
	v_add_u32_e32 v18, -1, v0
	s_movk_i32 s4, 0x201
	s_movk_i32 s5, 0x1ff
	v_cmp_gt_u32_e64 s[40:41], s4, v0
	v_cmp_gt_u32_e64 s[42:43], s5, v18
	v_mov_b32_e32 v18, 0x42c80000
	v_mov_b32_e32 v22, 0x3de38e39
	v_mov_b32_e32 v26, 0x3a3d6628
	v_mov_b32_e32 v1, 0
	s_add_i32 s4, s34, -3
	s_max_i32 s4, s4, 0
	s_mul_i32 s4, s4, 0x804
	s_add_i32 s4, s4, s38
	buffer_load_dword v29, v28, s[20:23], s4 offen nt
	s_add_i32 s4, s34, -2
	s_max_i32 s4, s4, 0
	s_mul_i32 s4, s4, 0x804
	s_add_i32 s4, s4, s38
	buffer_load_dword v2, v28, s[20:23], s4 offen nt
	s_add_i32 s5, s34, -2
	s_max_i32 s5, s5, 0
	s_mul_i32 s6, s5, 0x804
	s_add_i32 s6, s6, s35
	s_add_i32 s7, s6, 0x505014
	s_add_i32 s8, s6, 0x606018
	s_mul_i32 s9, s5, 0x180c
	s_add_i32 s9, s9, s33
	s_add_i32 s4, s34, -1
	s_max_i32 s4, s4, 0
	s_mul_i32 s4, s4, 0x804
	s_add_i32 s4, s4, s38
	buffer_load_dword v3, v28, s[20:23], s4 offen nt
	buffer_load_dwordx3 v[8:10], v27, s[24:27], s9 offen nt
	buffer_load_dword v4, v28, s[16:19], s7 offen nt
	buffer_load_dword v5, v28, s[16:19], s8 offen nt
	s_add_i32 s5, s34, -1
	s_max_i32 s5, s5, 0
	s_mul_i32 s6, s5, 0x804
	s_add_i32 s6, s6, s35
	s_add_i32 s7, s6, 0x505014
	s_add_i32 s8, s6, 0x606018
	s_mul_i32 s9, s5, 0x180c
	s_add_i32 s9, s9, s33
	s_add_i32 s4, s34, 0
	s_min_i32 s4, s4, 0x200
	s_mul_i32 s4, s4, 0x804
	s_add_i32 s4, s4, s38
	buffer_load_dword v16, v28, s[20:23], s4 offen nt
	buffer_load_dwordx3 v[12:14], v27, s[24:27], s9 offen nt
	buffer_load_dword v6, v28, s[16:19], s7 offen nt
	buffer_load_dword v7, v28, s[16:19], s8 offen nt
	s_add_i32 s5, s34, 0
	s_min_i32 s5, s5, 0x200
	s_mul_i32 s6, s5, 0x804
	s_add_i32 s6, s6, s35
	s_add_i32 s7, s6, 0x505014
	s_add_i32 s8, s6, 0x606018
	s_mul_i32 s9, s5, 0x180c
	s_add_i32 s9, s9, s33
	s_add_i32 s4, s34, 1
	s_min_i32 s4, s4, 0x200
	s_mul_i32 s4, s4, 0x804
	s_add_i32 s4, s4, s38
	buffer_load_dword v17, v28, s[20:23], s4 offen nt
	buffer_load_dwordx3 v[32:34], v27, s[24:27], s9 offen nt
	buffer_load_dword v20, v28, s[16:19], s7 offen nt
	buffer_load_dword v21, v28, s[16:19], s8 offen nt
	s_waitcnt vmcnt(12)
	s_add_i32 s4, s34, -3
	s_cmpk_lt_u32 s4, 0x201
	s_cselect_b64 s[12:13], s[40:41], 0
	v_cmp_eq_u32_e64 s[14:15], s37, v29
	s_and_b64 s[14:15], s[14:15], s[12:13]
	v_cndmask_b32_e64 v24, 0, 1, s[14:15]
	s_add_i32 s4, s34, -2
	s_cmpk_lt_u32 s4, 0x201
	s_cselect_b64 s[12:13], s[40:41], 0
	v_cmp_eq_u32_e64 s[14:15], s37, v2
	s_and_b64 s[14:15], s[14:15], s[12:13]
	v_cndmask_b32_e64 v25, 0, 1, s[14:15]
	s_nop 0
	v_or_b32_dpp v30, v24, v24 wave_shr:1 row_mask:0xf bank_mask:0xf bound_ctrl:1
	v_or_b32_dpp v31, v25, v25 wave_shr:1 row_mask:0xf bank_mask:0xf bound_ctrl:1
	s_nop 1
	v_or_b32_dpp v30, v24, v30 wave_shl:1 row_mask:0xf bank_mask:0xf bound_ctrl:1
	v_or_b32_dpp v31, v25, v31 wave_shl:1 row_mask:0xf bank_mask:0xf bound_ctrl:1
	s_nop 1
	v_or_b32_dpp v36, v30, v30 wave_shr:1 row_mask:0xf bank_mask:0xf bound_ctrl:1
	v_or_b32_dpp v37, v31, v31 wave_shr:1 row_mask:0xf bank_mask:0xf bound_ctrl:1
	s_nop 1
	v_or_b32_dpp v36, v30, v36 wave_shl:1 row_mask:0xf bank_mask:0xf bound_ctrl:1
	v_or_b32_dpp v37, v31, v37 wave_shl:1 row_mask:0xf bank_mask:0xf bound_ctrl:1
	v_mov_b32_e32 v24, 0
	v_mov_b32_e32 v25, 0
	s_waitcnt vmcnt(8)
	v_mov_b32_dpp v40, v8 wave_shr:1 row_mask:0xf bank_mask:0xf bound_ctrl:1
	v_mov_b32_dpp v41, v9 wave_shr:1 row_mask:0xf bank_mask:0xf bound_ctrl:1
	v_mov_b32_dpp v42, v10 wave_shr:1 row_mask:0xf bank_mask:0xf bound_ctrl:1
	v_mov_b32_dpp v44, v8 wave_shl:1 row_mask:0xf bank_mask:0xf bound_ctrl:1
	v_mov_b32_dpp v45, v9 wave_shl:1 row_mask:0xf bank_mask:0xf bound_ctrl:1
	v_mov_b32_dpp v46, v10 wave_shl:1 row_mask:0xf bank_mask:0xf bound_ctrl:1
	s_add_i32 s4, s34, -1
	s_cmpk_lt_u32 s4, 0x201
	s_cselect_b64 s[12:13], s[40:41], 0
	v_cmp_eq_u32_e64 s[14:15], s37, v3
	s_and_b64 s[14:15], s[14:15], s[12:13]
	v_cndmask_b32_e64 v30, 0, 1, s[14:15]
	v_pk_add_f32 v[38:39], v[8:9], v[40:41]
	v_pk_mul_f32 v[48:49], v[8:9], v[8:9] op_sel_hi:[0,1]
	v_or_b32_dpp v31, v30, v30 wave_shr:1 row_mask:0xf bank_mask:0xf bound_ctrl:1
	v_pk_mul_f32 v[50:51], v[8:9], v[10:11] op_sel_hi:[1,0]
	v_or_b32_dpp v31, v30, v31 wave_shl:1 row_mask:0xf bank_mask:0xf bound_ctrl:1
	v_mul_f32_e64 v52, v9, v9
	v_mul_f32_e64 v53, v10, v10
	v_or_b32_dpp v56, v31, v31 wave_shr:1 row_mask:0xf bank_mask:0xf bound_ctrl:1
	v_add_f32_e64 v54, v10, v42
	v_pk_add_f32 v[38:39], v[38:39], v[44:45]
	v_or_b32_dpp v56, v31, v56 wave_shl:1 row_mask:0xf bank_mask:0xf bound_ctrl:1
	v_or3_b32 v57, v56, v37, v36
	v_or3_b32 v57, v57, v24, v25
	s_add_i32 s4, s34, -4
	s_cmpk_lt_u32 s4, 0x1ff
	s_cselect_b64 s[12:13], s[42:43], 0
	v_cmp_ne_u32_e64 s[30:31], 0, v57
	s_and_b64 s[30:31], s[30:31], s[12:13]
	v_cndmask_b32_e64 v57, 0, 1.0, s[30:31]
	v_pk_fma_f32 v[48:49], v[40:41], v[40:41], v[48:49] op_sel_hi:[0,1,1]
	v_pk_fma_f32 v[50:51], v[40:41], v[42:43], v[50:51] op_sel_hi:[1,0,1]
	v_fma_f32 v52, v41, v41, v52
	v_fma_f32 v53, v42, v42, v53
	v_add_f32_dpp v55, v57, v57 wave_shr:1 row_mask:0xf bank_mask:0xf bound_ctrl:1
	v_add_f32_e64 v54, v54, v46
	v_pk_fma_f32 v[48:49], v[44:45], v[44:45], v[48:49] op_sel_hi:[0,1,1]
	v_pk_fma_f32 v[50:51], v[44:45], v[46:47], v[50:51] op_sel_hi:[1,0,1]
	v_fma_f32 v52, v45, v45, v52
	v_fma_f32 v53, v46, v46, v53
	v_add_f32_dpp v55, v57, v55 wave_shl:1 row_mask:0xf bank_mask:0xf bound_ctrl:1
	v_mov_b32_dpp v30, v4 wave_shr:1 row_mask:0xf bank_mask:0xf bound_ctrl:1
	v_mov_b32_dpp v31, v5 wave_shr:1 row_mask:0xf bank_mask:0xf bound_ctrl:1
	v_mov_b32_dpp v58, v4 wave_shl:1 row_mask:0xf bank_mask:0xf bound_ctrl:1
	v_mov_b32_dpp v59, v5 wave_shl:1 row_mask:0xf bank_mask:0xf bound_ctrl:1
	v_pk_mul_f32 v[60:61], v[4:5], v[8:9] op_sel_hi:[1,0]
	v_pk_mul_f32 v[64:65], v[4:5], v[8:9] op_sel:[0,1]
	v_pk_mul_f32 v[68:69], v[4:5], v[10:11] op_sel_hi:[1,0]
	v_pk_add_f32 v[72:73], v[4:5], v[30:31]
	v_pk_fma_f32 v[60:61], v[30:31], v[40:41], v[60:61] op_sel_hi:[1,0,1]
	v_pk_fma_f32 v[64:65], v[30:31], v[40:41], v[64:65] op_sel:[0,1,0]
	v_pk_fma_f32 v[68:69], v[30:31], v[42:43], v[68:69] op_sel_hi:[1,0,1]
	v_pk_add_f32 v[72:73], v[72:73], v[58:59]
	v_pk_fma_f32 v[60:61], v[58:59], v[44:45], v[60:61] op_sel_hi:[1,0,1]
	v_pk_fma_f32 v[64:65], v[58:59], v[44:45], v[64:65] op_sel:[0,1,0]
	v_pk_fma_f32 v[68:69], v[58:59], v[46:47], v[68:69] op_sel_hi:[1,0,1]
	s_barrier
	s_add_i32 s5, s34, 1
	s_min_i32 s5, s5, 0x200
	s_mul_i32 s6, s5, 0x804
	s_add_i32 s6, s6, s35
	s_add_i32 s7, s6, 0x505014
	s_add_i32 s8, s6, 0x606018
	s_mul_i32 s9, s5, 0x180c
	s_add_i32 s9, s9, s33
	s_add_i32 s4, s34, 2
	s_min_i32 s4, s4, 0x200
	s_mul_i32 s4, s4, 0x804
	s_add_i32 s4, s4, s38
	buffer_load_dword v25, v28, s[20:23], s4 offen nt
	buffer_load_dwordx3 v[76:78], v27, s[24:27], s9 offen nt
	buffer_load_dword v30, v28, s[16:19], s7 offen nt
	buffer_load_dword v31, v28, s[16:19], s8 offen nt
	s_waitcnt vmcnt(8)
	v_mov_b32_dpp v80, v12 wave_shr:1 row_mask:0xf bank_mask:0xf bound_ctrl:1
	v_mov_b32_dpp v81, v13 wave_shr:1 row_mask:0xf bank_mask:0xf bound_ctrl:1
	v_mov_b32_dpp v82, v14 wave_shr:1 row_mask:0xf bank_mask:0xf bound_ctrl:1
	v_mov_b32_dpp v84, v12 wave_shl:1 row_mask:0xf bank_mask:0xf bound_ctrl:1
	v_mov_b32_dpp v85, v13 wave_shl:1 row_mask:0xf bank_mask:0xf bound_ctrl:1
	v_mov_b32_dpp v86, v14 wave_shl:1 row_mask:0xf bank_mask:0xf bound_ctrl:1
	s_add_i32 s4, s34, 0
	s_cmpk_lt_u32 s4, 0x201
	s_cselect_b64 s[12:13], s[40:41], 0
	v_cmp_eq_u32_e64 s[14:15], s37, v16
	s_and_b64 s[14:15], s[14:15], s[12:13]
	v_cndmask_b32_e64 v57, 0, 1, s[14:15]
	v_pk_add_f32 v[58:59], v[12:13], v[80:81]
	v_pk_mul_f32 v[62:63], v[12:13], v[12:13] op_sel_hi:[0,1]
	v_or_b32_dpp v88, v57, v57 wave_shr:1 row_mask:0xf bank_mask:0xf bound_ctrl:1
	v_pk_mul_f32 v[66:67], v[12:13], v[14:15] op_sel_hi:[1,0]
	v_or_b32_dpp v88, v57, v88 wave_shl:1 row_mask:0xf bank_mask:0xf bound_ctrl:1
	v_mul_f32_e64 v70, v13, v13
	v_mul_f32_e64 v71, v14, v14
	v_or_b32_dpp v89, v88, v88 wave_shr:1 row_mask:0xf bank_mask:0xf bound_ctrl:1
	v_add_f32_e64 v74, v14, v82
	v_pk_add_f32 v[58:59], v[58:59], v[84:85]
	v_or_b32_dpp v89, v88, v89 wave_shl:1 row_mask:0xf bank_mask:0xf bound_ctrl:1
	v_or3_b32 v57, v89, v56, v37
	v_or3_b32 v57, v57, v36, v24
	s_add_i32 s4, s34, -3
	s_cmpk_lt_u32 s4, 0x1ff
	s_cselect_b64 s[12:13], s[42:43], 0
	v_cmp_ne_u32_e64 s[30:31], 0, v57
	s_and_b64 s[30:31], s[30:31], s[12:13]
	v_cndmask_b32_e64 v57, 0, 1.0, s[30:31]
	v_pk_fma_f32 v[62:63], v[80:81], v[80:81], v[62:63] op_sel_hi:[0,1,1]
	v_pk_fma_f32 v[66:67], v[80:81], v[82:83], v[66:67] op_sel_hi:[1,0,1]
	v_fma_f32 v70, v81, v81, v70
	v_fma_f32 v71, v82, v82, v71
	v_add_f32_dpp v75, v57, v57 wave_shr:1 row_mask:0xf bank_mask:0xf bound_ctrl:1
	v_add_f32_e64 v74, v74, v86
	v_pk_fma_f32 v[62:63], v[84:85], v[84:85], v[62:63] op_sel_hi:[0,1,1]
	v_pk_fma_f32 v[66:67], v[84:85], v[86:87], v[66:67] op_sel_hi:[1,0,1]
	v_fma_f32 v70, v85, v85, v70
	v_fma_f32 v71, v86, v86, v71
	v_add_f32_dpp v75, v57, v75 wave_shl:1 row_mask:0xf bank_mask:0xf bound_ctrl:1
	v_mov_b32_dpp v92, v6 wave_shr:1 row_mask:0xf bank_mask:0xf bound_ctrl:1
	v_mov_b32_dpp v93, v7 wave_shr:1 row_mask:0xf bank_mask:0xf bound_ctrl:1
	v_mov_b32_dpp v96, v6 wave_shl:1 row_mask:0xf bank_mask:0xf bound_ctrl:1
	v_mov_b32_dpp v97, v7 wave_shl:1 row_mask:0xf bank_mask:0xf bound_ctrl:1
	v_pk_mul_f32 v[90:91], v[6:7], v[12:13] op_sel_hi:[1,0]
	v_pk_mul_f32 v[94:95], v[6:7], v[12:13] op_sel:[0,1]
	v_pk_mul_f32 v[98:99], v[6:7], v[14:15] op_sel_hi:[1,0]
	v_pk_add_f32 v[102:103], v[6:7], v[92:93]
	v_pk_fma_f32 v[90:91], v[92:93], v[80:81], v[90:91] op_sel_hi:[1,0,1]
	v_pk_fma_f32 v[94:95], v[92:93], v[80:81], v[94:95] op_sel:[0,1,0]
	v_pk_fma_f32 v[98:99], v[92:93], v[82:83], v[98:99] op_sel_hi:[1,0,1]
	v_pk_add_f32 v[102:103], v[102:103], v[96:97]
	v_pk_fma_f32 v[90:91], v[96:97], v[84:85], v[90:91] op_sel_hi:[1,0,1]
	v_pk_fma_f32 v[94:95], v[96:97], v[84:85], v[94:95] op_sel:[0,1,0]
	v_pk_fma_f32 v[98:99], v[96:97], v[86:87], v[98:99] op_sel_hi:[1,0,1]
	s_barrier
	s_add_i32 s5, s34, 2
	s_min_i32 s5, s5, 0x200
	s_mul_i32 s6, s5, 0x804
	s_add_i32 s6, s6, s35
	s_add_i32 s7, s6, 0x505014
	s_add_i32 s8, s6, 0x606018
	s_mul_i32 s9, s5, 0x180c
	s_add_i32 s9, s9, s33
	s_add_i32 s4, s34, 3
	s_min_i32 s4, s4, 0x200
	s_mul_i32 s4, s4, 0x804
	s_add_i32 s4, s4, s38
	buffer_load_dword v24, v28, s[20:23], s4 offen nt
	buffer_load_dwordx3 v[104:106], v27, s[24:27], s9 offen nt
	buffer_load_dword v92, v28, s[16:19], s7 offen nt
	buffer_load_dword v93, v28, s[16:19], s8 offen nt
	s_waitcnt vmcnt(8)
	v_mov_b32_dpp v108, v32 wave_shr:1 row_mask:0xf bank_mask:0xf bound_ctrl:1
	v_mov_b32_dpp v109, v33 wave_shr:1 row_mask:0xf bank_mask:0xf bound_ctrl:1
	v_mov_b32_dpp v110, v34 wave_shr:1 row_mask:0xf bank_mask:0xf bound_ctrl:1
	v_mov_b32_dpp v112, v32 wave_shl:1 row_mask:0xf bank_mask:0xf bound_ctrl:1
	v_mov_b32_dpp v113, v33 wave_shl:1 row_mask:0xf bank_mask:0xf bound_ctrl:1
	v_mov_b32_dpp v114, v34 wave_shl:1 row_mask:0xf bank_mask:0xf bound_ctrl:1
	s_add_i32 s4, s34, 1
	s_cmpk_lt_u32 s4, 0x201
	s_cselect_b64 s[12:13], s[40:41], 0
	v_cmp_eq_u32_e64 s[14:15], s37, v17
	s_and_b64 s[14:15], s[14:15], s[12:13]
	v_cndmask_b32_e64 v29, 0, 1, s[14:15]
	v_pk_add_f32 v[96:97], v[32:33], v[108:109]
	v_pk_mul_f32 v[100:101], v[32:33], v[32:33] op_sel_hi:[0,1]
	v_or_b32_dpp v57, v29, v29 wave_shr:1 row_mask:0xf bank_mask:0xf bound_ctrl:1
	v_pk_mul_f32 v[116:117], v[32:33], v[34:35] op_sel_hi:[1,0]
	v_or_b32_dpp v57, v29, v57 wave_shl:1 row_mask:0xf bank_mask:0xf bound_ctrl:1
	v_mul_f32_e64 v118, v33, v33
	v_mul_f32_e64 v119, v34, v34
	v_or_b32_dpp v88, v57, v57 wave_shr:1 row_mask:0xf bank_mask:0xf bound_ctrl:1
	v_add_f32_e64 v120, v34, v110
	v_pk_add_f32 v[96:97], v[96:97], v[112:113]
	v_or_b32_dpp v88, v57, v88 wave_shl:1 row_mask:0xf bank_mask:0xf bound_ctrl:1
	v_or3_b32 v29, v88, v89, v56
	v_or3_b32 v29, v29, v37, v36
	s_add_i32 s4, s34, -2
	s_cmpk_lt_u32 s4, 0x1ff
	s_cselect_b64 s[12:13], s[42:43], 0
	v_cmp_ne_u32_e64 s[30:31], 0, v29
	s_and_b64 s[30:31], s[30:31], s[12:13]
	v_cndmask_b32_e64 v29, 0, 1.0, s[30:31]
	v_pk_fma_f32 v[100:101], v[108:109], v[108:109], v[100:101] op_sel_hi:[0,1,1]
	v_pk_fma_f32 v[116:117], v[108:109], v[110:111], v[116:117] op_sel_hi:[1,0,1]
	v_fma_f32 v118, v109, v109, v118
	v_fma_f32 v119, v110, v110, v119
	v_add_f32_dpp v121, v29, v29 wave_shr:1 row_mask:0xf bank_mask:0xf bound_ctrl:1
	v_add_f32_e64 v120, v120, v114
	v_pk_fma_f32 v[100:101], v[112:113], v[112:113], v[100:101] op_sel_hi:[0,1,1]
	v_pk_fma_f32 v[116:117], v[112:113], v[114:115], v[116:117] op_sel_hi:[1,0,1]
	v_fma_f32 v118, v113, v113, v118
	v_fma_f32 v119, v114, v114, v119
	v_add_f32_dpp v121, v29, v121 wave_shl:1 row_mask:0xf bank_mask:0xf bound_ctrl:1
	v_pk_add_f32 v[124:125], v[58:59], v[96:97]
	v_pk_add_f32 v[122:123], v[38:39], v[124:125]
	v_pk_add_f32 v[38:39], v[62:63], v[100:101]
	v_pk_add_f32 v[58:59], v[48:49], v[38:39]
	v_pk_add_f32 v[48:49], v[66:67], v[116:117]
	v_pk_add_f32 v[62:63], v[50:51], v[48:49]
	v_pk_add_f32 v[50:51], v[70:71], v[118:119]
	v_pk_add_f32 v[66:67], v[52:53], v[50:51]
	v_pk_add_f32 v[52:53], v[74:75], v[120:121]
	v_pk_add_f32 v[70:71], v[54:55], v[52:53]
	v_mul_f32_e64 v128, v122, v22
	v_mul_f32_e64 v129, v123, v22
	v_mul_f32_e64 v130, v70, v22
	v_fma_f32 v29, v58, v22, v26
	v_mul_f32_e64 v57, v59, v22
	v_mul_f32_e64 v54, v62, v22
	v_fma_f32 v55, v66, v22, v26
	v_mul_f32_e64 v74, v63, v22
	v_fma_f32 v75, v67, v22, v26
	v_fma_f32 v29, -v128, v128, v29
	v_fma_f32 v57, -v128, v129, v57
	v_fma_f32 v54, -v128, v130, v54
	v_fma_f32 v55, -v129, v129, v55
	v_fma_f32 v74, -v129, v130, v74
	v_fma_f32 v75, -v130, v130, v75
	v_mul_f32_e64 v126, v74, v74
	v_mul_f32_e64 v127, v57, v75
	v_mul_f32_e64 v140, v54, v55
	v_mul_f32_e64 v141, v54, v54
	v_mul_f32_e64 v142, v29, v74
	v_mul_f32_e64 v143, v57, v57
	v_fma_f32 v126, v55, v75, -v126
	v_fma_f32 v127, v54, v74, -v127
	v_fma_f32 v140, v57, v74, -v140
	v_fma_f32 v141, v29, v75, -v141
	v_fma_f32 v142, v57, v54, -v142
	v_fma_f32 v143, v29, v55, -v143
	v_mul_f32_e64 v144, v29, v126
	v_fma_f32 v144, v57, v127, v144
	v_fma_f32 v144, v54, v140, v144
	v_rcp_f32_e32 v144, v144
	v_cmp_ne_u32_e64 vcc, s37, v2
	v_mul_f32_e64 v144, v144, v22
	v_cndmask_b32_e64 v144, 0, v144, s[30:31]
	v_cndmask_b32_e64 v29, 0, v18, vcc
	v_cndmask_b32_e64 v137, 0, v22, s[30:31]
	v_mul_f32_e64 v131, v126, v144
	v_mul_f32_e64 v132, v127, v144
	v_mul_f32_e64 v133, v140, v144
	v_mul_f32_e64 v134, v141, v144
	v_mul_f32_e64 v135, v142, v144
	v_mul_f32_e64 v136, v143, v144
	v_add_f32_e64 v138, v71, v29
	v_mov_b32_e32 v139, v2
	ds_write_b128 v23, v[128:131]
	ds_write_b128 v23, v[132:135] offset:1024
	ds_write_b128 v23, v[136:139] offset:2048
	v_mov_b32_dpp v54, v20 wave_shr:1 row_mask:0xf bank_mask:0xf bound_ctrl:1
	v_mov_b32_dpp v55, v21 wave_shr:1 row_mask:0xf bank_mask:0xf bound_ctrl:1
	v_mov_b32_dpp v58, v20 wave_shl:1 row_mask:0xf bank_mask:0xf bound_ctrl:1
	v_mov_b32_dpp v59, v21 wave_shl:1 row_mask:0xf bank_mask:0xf bound_ctrl:1
	v_pk_mul_f32 v[140:141], v[20:21], v[32:33] op_sel_hi:[1,0]
	v_pk_mul_f32 v[144:145], v[20:21], v[32:33] op_sel:[0,1]
	v_pk_mul_f32 v[148:149], v[20:21], v[34:35] op_sel_hi:[1,0]
	v_pk_add_f32 v[152:153], v[20:21], v[54:55]
	v_pk_fma_f32 v[140:141], v[54:55], v[108:109], v[140:141] op_sel_hi:[1,0,1]
	v_pk_fma_f32 v[144:145], v[54:55], v[108:109], v[144:145] op_sel:[0,1,0]
	v_pk_fma_f32 v[148:149], v[54:55], v[110:111], v[148:149] op_sel_hi:[1,0,1]
	v_pk_add_f32 v[152:153], v[152:153], v[58:59]
	v_pk_fma_f32 v[140:141], v[58:59], v[112:113], v[140:141] op_sel_hi:[1,0,1]
	v_pk_fma_f32 v[144:145], v[58:59], v[112:113], v[144:145] op_sel:[0,1,0]
	v_pk_fma_f32 v[148:149], v[58:59], v[114:115], v[148:149] op_sel_hi:[1,0,1]
	s_waitcnt lgkmcnt(0)
	s_barrier
	s_add_i32 s5, s34, 3
	s_min_i32 s5, s5, 0x200
	s_mul_i32 s6, s5, 0x804
	s_add_i32 s6, s6, s35
	s_add_i32 s7, s6, 0x505014
	s_add_i32 s8, s6, 0x606018
	s_mul_i32 s9, s5, 0x180c
	s_add_i32 s9, s9, s33
	s_add_i32 s4, s34, 4
	s_min_i32 s4, s4, 0x200
	s_mul_i32 s4, s4, 0x804
	s_add_i32 s4, s4, s38
	buffer_load_dword v2, v28, s[20:23], s4 offen nt
	buffer_load_dwordx3 v[156:158], v27, s[24:27], s9 offen nt
	buffer_load_dword v54, v28, s[16:19], s7 offen nt
	buffer_load_dword v55, v28, s[16:19], s8 offen nt
	v_pk_add_f32 v[58:59], v[102:103], v[152:153]
	v_pk_add_f32 v[62:63], v[72:73], v[58:59]
	v_pk_add_f32 v[66:67], v[90:91], v[140:141]
	v_pk_add_f32 v[72:73], v[60:61], v[66:67]
	v_pk_add_f32 v[70:71], v[94:95], v[144:145]
	v_pk_add_f32 v[60:61], v[64:65], v[70:71]
	v_pk_add_f32 v[74:75], v[98:99], v[148:149]
	v_pk_add_f32 v[64:65], v[68:69], v[74:75]
	v_pk_fma_f32 v[72:73], v[128:129], v[62:63], v[72:73] op_sel_hi:[0,1,1] neg_lo:[1,0,0] neg_hi:[1,0,0]
	v_pk_fma_f32 v[60:61], v[128:129], v[62:63], v[60:61] op_sel:[1,0,0] neg_lo:[1,0,0] neg_hi:[1,0,0]
	v_pk_fma_f32 v[64:65], v[130:131], v[62:63], v[64:65] op_sel_hi:[0,1,1] neg_lo:[1,0,0] neg_hi:[1,0,0]
	v_pk_mul_f32 v[90:91], v[130:131], v[72:73] op_sel:[1,0]
	v_pk_mul_f32 v[94:95], v[132:133], v[72:73] op_sel_hi:[0,1]
	v_pk_mul_f32 v[98:99], v[132:133], v[72:73] op_sel:[1,0]
	v_pk_fma_f32 v[90:91], v[132:133], v[60:61], v[90:91] op_sel_hi:[0,1,1]
	v_pk_fma_f32 v[94:95], v[134:135], v[60:61], v[94:95] op_sel_hi:[0,1,1]
	v_pk_fma_f32 v[98:99], v[134:135], v[60:61], v[98:99] op_sel:[1,0,0]
	v_pk_fma_f32 v[90:91], v[132:133], v[64:65], v[90:91] op_sel:[1,0,0]
	v_pk_fma_f32 v[94:95], v[134:135], v[64:65], v[94:95] op_sel:[1,0,0]
	v_pk_fma_f32 v[98:99], v[136:137], v[64:65], v[98:99] op_sel_hi:[0,1,1]
	v_pk_mul_f32 v[68:69], v[128:129], v[90:91] op_sel_hi:[0,1]
	v_pk_fma_f32 v[68:69], v[128:129], v[94:95], v[68:69] op_sel:[1,0,0]
	v_pk_fma_f32 v[68:69], v[130:131], v[98:99], v[68:69] op_sel_hi:[0,1,1]
	v_pk_fma_f32 v[68:69], v[136:137], v[62:63], v[68:69] op_sel:[1,0,0] neg_lo:[0,0,1] neg_hi:[0,0,1]
	s_waitcnt vmcnt(8)
	v_mov_b32_dpp v8, v76 wave_shr:1 row_mask:0xf bank_mask:0xf bound_ctrl:1
	v_mov_b32_dpp v9, v77 wave_shr:1 row_mask:0xf bank_mask:0xf bound_ctrl:1
	v_mov_b32_dpp v10, v78 wave_shr:1 row_mask:0xf bank_mask:0xf bound_ctrl:1
	v_mov_b32_dpp v40, v76 wave_shl:1 row_mask:0xf bank_mask:0xf bound_ctrl:1
	v_mov_b32_dpp v41, v77 wave_shl:1 row_mask:0xf bank_mask:0xf bound_ctrl:1
	v_mov_b32_dpp v42, v78 wave_shl:1 row_mask:0xf bank_mask:0xf bound_ctrl:1
	s_add_i32 s4, s34, 2
	s_cmpk_lt_u32 s4, 0x201
	s_cselect_b64 s[12:13], s[40:41], 0
	v_cmp_eq_u32_e64 s[14:15], s37, v25
	s_and_b64 s[14:15], s[14:15], s[12:13]
	v_cndmask_b32_e64 v29, 0, 1, s[14:15]
	v_pk_add_f32 v[4:5], v[76:77], v[8:9]
	v_pk_mul_f32 v[44:45], v[76:77], v[76:77] op_sel_hi:[0,1]
	v_or_b32_dpp v36, v29, v29 wave_shr:1 row_mask:0xf bank_mask:0xf bound_ctrl:1
	v_pk_mul_f32 v[46:47], v[76:77], v[78:79] op_sel_hi:[1,0]
	v_or_b32_dpp v36, v29, v36 wave_shl:1 row_mask:0xf bank_mask:0xf bound_ctrl:1
	v_mul_f32_e64 v60, v77, v77
	v_mul_f32_e64 v61, v78, v78
	v_or_b32_dpp v57, v36, v36 wave_shr:1 row_mask:0xf bank_mask:0xf bound_ctrl:1
	v_add_f32_e64 v62, v78, v10
	v_pk_add_f32 v[4:5], v[4:5], v[40:41]
	v_or_b32_dpp v57, v36, v57 wave_shl:1 row_mask:0xf bank_mask:0xf bound_ctrl:1
	v_or3_b32 v29, v57, v88, v89
	v_or3_b32 v29, v29, v56, v37
	s_add_i32 s4, s34, -1
	s_cmpk_lt_u32 s4, 0x1ff
	s_cselect_b64 s[12:13], s[42:43], 0
	v_cmp_ne_u32_e64 s[30:31], 0, v29
	s_and_b64 s[30:31], s[30:31], s[12:13]
	v_cndmask_b32_e64 v29, 0, 1.0, s[30:31]
	v_pk_fma_f32 v[44:45], v[8:9], v[8:9], v[44:45] op_sel_hi:[0,1,1]
	v_pk_fma_f32 v[46:47], v[8:9], v[10:11], v[46:47] op_sel_hi:[1,0,1]
	v_fma_f32 v60, v9, v9, v60
	v_fma_f32 v61, v10, v10, v61
	v_add_f32_dpp v63, v29, v29 wave_shr:1 row_mask:0xf bank_mask:0xf bound_ctrl:1
	v_add_f32_e64 v62, v62, v42
	v_pk_fma_f32 v[44:45], v[40:41], v[40:41], v[44:45] op_sel_hi:[0,1,1]
	v_pk_fma_f32 v[46:47], v[40:41], v[42:43], v[46:47] op_sel_hi:[1,0,1]
	v_fma_f32 v60, v41, v41, v60
	v_fma_f32 v61, v42, v42, v61
	v_add_f32_dpp v63, v29, v63 wave_shl:1 row_mask:0xf bank_mask:0xf bound_ctrl:1
	v_pk_add_f32 v[64:65], v[124:125], v[4:5]
	v_pk_add_f32 v[72:73], v[38:39], v[44:45]
	v_pk_add_f32 v[38:39], v[48:49], v[46:47]
	v_pk_add_f32 v[48:49], v[50:51], v[60:61]
	v_pk_add_f32 v[50:51], v[52:53], v[62:63]
	v_mul_f32_e64 v124, v64, v22
	v_mul_f32_e64 v125, v65, v22
	v_mul_f32_e64 v126, v50, v22
	v_fma_f32 v29, v72, v22, v26
	v_mul_f32_e64 v36, v73, v22
	v_mul_f32_e64 v52, v38, v22
	v_fma_f32 v53, v48, v22, v26
	v_mul_f32_e64 v102, v39, v22
	v_fma_f32 v103, v49, v22, v26
	v_fma_f32 v29, -v124, v124, v29
	v_fma_f32 v36, -v124, v125, v36
	v_fma_f32 v52, -v124, v126, v52
	v_fma_f32 v53, -v125, v125, v53
	v_fma_f32 v102, -v125, v126, v102
	v_fma_f32 v103, -v126, v126, v103
	v_mul_f32_e64 v122, v102, v102
	v_mul_f32_e64 v123, v36, v103
	v_mul_f32_e64 v136, v52, v53
	v_mul_f32_e64 v137, v52, v52
	v_mul_f32_e64 v138, v29, v102
	v_mul_f32_e64 v139, v36, v36
	v_fma_f32 v122, v53, v103, -v122
	v_fma_f32 v123, v52, v102, -v123
	v_fma_f32 v136, v36, v102, -v136
	v_fma_f32 v137, v29, v103, -v137
	v_fma_f32 v138, v36, v52, -v138
	v_fma_f32 v139, v29, v53, -v139
	v_mul_f32_e64 v142, v29, v122
	v_fma_f32 v142, v36, v123, v142
	v_fma_f32 v142, v52, v136, v142
	v_rcp_f32_e32 v142, v142
	v_cmp_ne_u32_e64 vcc, s37, v3
	v_mul_f32_e64 v142, v142, v22
	v_cndmask_b32_e64 v142, 0, v142, s[30:31]
	v_cndmask_b32_e64 v29, 0, v18, vcc
	v_cndmask_b32_e64 v133, 0, v22, s[30:31]
	v_mul_f32_e64 v127, v122, v142
	v_mul_f32_e64 v128, v123, v142
	v_mul_f32_e64 v129, v136, v142
	v_mul_f32_e64 v130, v137, v142
	v_mul_f32_e64 v131, v138, v142
	v_mul_f32_e64 v132, v139, v142
	v_add_f32_e64 v134, v51, v29
	v_mov_b32_e32 v135, v3
	ds_write_b128 v23, v[124:127] offset:3072
	ds_write_b128 v23, v[128:131] offset:4096
	ds_write_b128 v23, v[132:135] offset:5120
	v_mov_b32_dpp v36, v30 wave_shr:1 row_mask:0xf bank_mask:0xf bound_ctrl:1
	v_mov_b32_dpp v37, v31 wave_shr:1 row_mask:0xf bank_mask:0xf bound_ctrl:1
	v_mov_b32_dpp v48, v30 wave_shl:1 row_mask:0xf bank_mask:0xf bound_ctrl:1
	v_mov_b32_dpp v49, v31 wave_shl:1 row_mask:0xf bank_mask:0xf bound_ctrl:1
	v_pk_mul_f32 v[38:39], v[30:31], v[76:77] op_sel_hi:[1,0]
	v_pk_mul_f32 v[50:51], v[30:31], v[76:77] op_sel:[0,1]
	v_pk_mul_f32 v[102:103], v[30:31], v[78:79] op_sel_hi:[1,0]
	v_pk_add_f32 v[122:123], v[30:31], v[36:37]
	v_pk_fma_f32 v[38:39], v[36:37], v[8:9], v[38:39] op_sel_hi:[1,0,1]
	v_pk_fma_f32 v[50:51], v[36:37], v[8:9], v[50:51] op_sel:[0,1,0]
	v_pk_fma_f32 v[102:103], v[36:37], v[10:11], v[102:103] op_sel_hi:[1,0,1]
	v_pk_add_f32 v[122:123], v[122:123], v[48:49]
	v_pk_fma_f32 v[38:39], v[48:49], v[40:41], v[38:39] op_sel_hi:[1,0,1]
	v_pk_fma_f32 v[50:51], v[48:49], v[40:41], v[50:51] op_sel:[0,1,0]
	v_pk_fma_f32 v[102:103], v[48:49], v[42:43], v[102:103] op_sel_hi:[1,0,1]
	s_waitcnt lgkmcnt(0)
	s_barrier
	s_add_i32 s5, s34, 4
	s_min_i32 s5, s5, 0x200
	s_mul_i32 s6, s5, 0x804
	s_add_i32 s6, s6, s35
	s_add_i32 s7, s6, 0x505014
	s_add_i32 s8, s6, 0x606018
	s_mul_i32 s9, s5, 0x180c
	s_add_i32 s9, s9, s33
	s_add_i32 s4, s34, 5
	s_min_i32 s4, s4, 0x200
	s_mul_i32 s4, s4, 0x804
	s_add_i32 s4, s4, s38
	buffer_load_dword v3, v28, s[20:23], s4 offen nt
	buffer_load_dwordx3 v[136:138], v27, s[24:27], s9 offen nt
	buffer_load_dword v36, v28, s[16:19], s7 offen nt
	buffer_load_dword v37, v28, s[16:19], s8 offen nt
	v_pk_add_f32 v[48:49], v[58:59], v[122:123]
	v_pk_add_f32 v[58:59], v[66:67], v[38:39]
	v_pk_add_f32 v[66:67], v[70:71], v[50:51]
	v_pk_add_f32 v[70:71], v[74:75], v[102:103]
	v_pk_fma_f32 v[58:59], v[124:125], v[48:49], v[58:59] op_sel_hi:[0,1,1] neg_lo:[1,0,0] neg_hi:[1,0,0]
	v_pk_fma_f32 v[66:67], v[124:125], v[48:49], v[66:67] op_sel:[1,0,0] neg_lo:[1,0,0] neg_hi:[1,0,0]
	v_pk_fma_f32 v[70:71], v[126:127], v[48:49], v[70:71] op_sel_hi:[0,1,1] neg_lo:[1,0,0] neg_hi:[1,0,0]
	v_pk_mul_f32 v[52:53], v[126:127], v[58:59] op_sel:[1,0]
	v_pk_mul_f32 v[64:65], v[128:129], v[58:59] op_sel_hi:[0,1]
	v_pk_mul_f32 v[72:73], v[128:129], v[58:59] op_sel:[1,0]
	v_pk_fma_f32 v[52:53], v[128:129], v[66:67], v[52:53] op_sel_hi:[0,1,1]
	v_pk_fma_f32 v[64:65], v[130:131], v[66:67], v[64:65] op_sel_hi:[0,1,1]
	v_pk_fma_f32 v[72:73], v[130:131], v[66:67], v[72:73] op_sel:[1,0,0]
	v_pk_fma_f32 v[52:53], v[128:129], v[70:71], v[52:53] op_sel:[1,0,0]
	v_pk_fma_f32 v[64:65], v[130:131], v[70:71], v[64:65] op_sel:[1,0,0]
	v_pk_fma_f32 v[72:73], v[132:133], v[70:71], v[72:73] op_sel_hi:[0,1,1]
	v_pk_mul_f32 v[74:75], v[124:125], v[52:53] op_sel_hi:[0,1]
	v_pk_fma_f32 v[74:75], v[124:125], v[64:65], v[74:75] op_sel:[1,0,0]
	v_pk_fma_f32 v[74:75], v[126:127], v[72:73], v[74:75] op_sel_hi:[0,1,1]
	v_pk_fma_f32 v[74:75], v[132:133], v[48:49], v[74:75] op_sel:[1,0,0] neg_lo:[0,0,1] neg_hi:[0,0,1]
	s_waitcnt vmcnt(8)
	v_mov_b32_dpp v12, v104 wave_shr:1 row_mask:0xf bank_mask:0xf bound_ctrl:1
	v_mov_b32_dpp v13, v105 wave_shr:1 row_mask:0xf bank_mask:0xf bound_ctrl:1
	v_mov_b32_dpp v14, v106 wave_shr:1 row_mask:0xf bank_mask:0xf bound_ctrl:1
	v_mov_b32_dpp v80, v104 wave_shl:1 row_mask:0xf bank_mask:0xf bound_ctrl:1
	v_mov_b32_dpp v81, v105 wave_shl:1 row_mask:0xf bank_mask:0xf bound_ctrl:1
	v_mov_b32_dpp v82, v106 wave_shl:1 row_mask:0xf bank_mask:0xf bound_ctrl:1
	s_add_i32 s4, s34, 3
	s_cmpk_lt_u32 s4, 0x201
	s_cselect_b64 s[12:13], s[40:41], 0
	v_cmp_eq_u32_e64 s[14:15], s37, v24
	s_and_b64 s[14:15], s[14:15], s[12:13]
	v_cndmask_b32_e64 v29, 0, 1, s[14:15]
	v_pk_add_f32 v[6:7], v[104:105], v[12:13]
	v_pk_mul_f32 v[48:49], v[104:105], v[104:105] op_sel_hi:[0,1]
	v_or_b32_dpp v84, v29, v29 wave_shr:1 row_mask:0xf bank_mask:0xf bound_ctrl:1
	v_pk_mul_f32 v[58:59], v[104:105], v[106:107] op_sel_hi:[1,0]
	v_or_b32_dpp v84, v29, v84 wave_shl:1 row_mask:0xf bank_mask:0xf bound_ctrl:1
	v_mul_f32_e64 v66, v105, v105
	v_mul_f32_e64 v67, v106, v106
	v_or_b32_dpp v85, v84, v84 wave_shr:1 row_mask:0xf bank_mask:0xf bound_ctrl:1
	v_add_f32_e64 v70, v106, v14
	v_pk_add_f32 v[6:7], v[6:7], v[80:81]
	v_or_b32_dpp v85, v84, v85 wave_shl:1 row_mask:0xf bank_mask:0xf bound_ctrl:1
	v_or3_b32 v29, v85, v57, v88
	v_or3_b32 v29, v29, v89, v56
	s_add_i32 s4, s34, 0
	s_cmpk_lt_u32 s4, 0x1ff
	s_cselect_b64 s[12:13], s[42:43], 0
	v_cmp_ne_u32_e64 s[30:31], 0, v29
	s_and_b64 s[30:31], s[30:31], s[12:13]
	v_cndmask_b32_e64 v29, 0, 1.0, s[30:31]
	v_pk_fma_f32 v[48:49], v[12:13], v[12:13], v[48:49] op_sel_hi:[0,1,1]
	v_pk_fma_f32 v[58:59], v[12:13], v[14:15], v[58:59] op_sel_hi:[1,0,1]
	v_fma_f32 v66, v13, v13, v66
	v_fma_f32 v67, v14, v14, v67
	v_add_f32_dpp v71, v29, v29 wave_shr:1 row_mask:0xf bank_mask:0xf bound_ctrl:1
	v_add_f32_e64 v70, v70, v82
	v_pk_fma_f32 v[48:49], v[80:81], v[80:81], v[48:49] op_sel_hi:[0,1,1]
	v_pk_fma_f32 v[58:59], v[80:81], v[82:83], v[58:59] op_sel_hi:[1,0,1]
	v_fma_f32 v66, v81, v81, v66
	v_fma_f32 v67, v82, v82, v67
	v_add_f32_dpp v71, v29, v71 wave_shl:1 row_mask:0xf bank_mask:0xf bound_ctrl:1
	v_pk_add_f32 v[86:87], v[4:5], v[6:7]
	v_pk_add_f32 v[124:125], v[96:97], v[86:87]
	v_pk_add_f32 v[126:127], v[44:45], v[48:49]
	v_pk_add_f32 v[4:5], v[100:101], v[126:127]
	v_pk_add_f32 v[130:131], v[46:47], v[58:59]
	v_pk_add_f32 v[44:45], v[116:117], v[130:131]
	v_pk_add_f32 v[96:97], v[60:61], v[66:67]
	v_pk_add_f32 v[46:47], v[118:119], v[96:97]
	v_pk_add_f32 v[118:119], v[62:63], v[70:71]
	v_pk_add_f32 v[60:61], v[120:121], v[118:119]
	v_mul_f32_e64 v132, v124, v22
	v_mul_f32_e64 v133, v125, v22
	v_mul_f32_e64 v134, v60, v22
	v_fma_f32 v29, v4, v22, v26
	v_mul_f32_e64 v84, v5, v22
	v_mul_f32_e64 v62, v44, v22
	v_fma_f32 v63, v46, v22, v26
	v_mul_f32_e64 v100, v45, v22
	v_fma_f32 v101, v47, v22, v26
	v_fma_f32 v29, -v132, v132, v29
	v_fma_f32 v84, -v132, v133, v84
	v_fma_f32 v62, -v132, v134, v62
	v_fma_f32 v63, -v133, v133, v63
	v_fma_f32 v100, -v133, v134, v100
	v_fma_f32 v101, -v134, v134, v101
	v_mul_f32_e64 v116, v100, v100
	v_mul_f32_e64 v117, v84, v101
	v_mul_f32_e64 v120, v62, v63
	v_mul_f32_e64 v121, v62, v62
	v_mul_f32_e64 v128, v29, v100
	v_mul_f32_e64 v129, v84, v84
	v_fma_f32 v116, v63, v101, -v116
	v_fma_f32 v117, v62, v100, -v117
	v_fma_f32 v120, v84, v100, -v120
	v_fma_f32 v121, v29, v101, -v121
	v_fma_f32 v128, v84, v62, -v128
	v_fma_f32 v129, v29, v63, -v129
	v_mul_f32_e64 v142, v29, v116
	v_fma_f32 v142, v84, v117, v142
	v_fma_f32 v142, v62, v120, v142
	v_rcp_f32_e32 v142, v142
	v_cmp_ne_u32_e64 vcc, s37, v16
	v_mul_f32_e64 v142, v142, v22
	v_cndmask_b32_e64 v142, 0, v142, s[30:31]
	v_cndmask_b32_e64 v29, 0, v18, vcc
	v_cndmask_b32_e64 v165, 0, v22, s[30:31]
	v_mul_f32_e64 v135, v116, v142
	v_mul_f32_e64 v160, v117, v142
	v_mul_f32_e64 v161, v120, v142
	v_mul_f32_e64 v162, v121, v142
	v_mul_f32_e64 v163, v128, v142
	v_mul_f32_e64 v164, v129, v142
	v_add_f32_e64 v166, v61, v29
	v_mov_b32_e32 v167, v16
	ds_write_b128 v23, v[132:135]
	ds_write_b128 v23, v[160:163] offset:1024
	ds_write_b128 v23, v[164:167] offset:2048
	v_mov_b32_dpp v46, v92 wave_shr:1 row_mask:0xf bank_mask:0xf bound_ctrl:1
	v_mov_b32_dpp v47, v93 wave_shr:1 row_mask:0xf bank_mask:0xf bound_ctrl:1
	v_mov_b32_dpp v62, v92 wave_shl:1 row_mask:0xf bank_mask:0xf bound_ctrl:1
	v_mov_b32_dpp v63, v93 wave_shl:1 row_mask:0xf bank_mask:0xf bound_ctrl:1
	v_pk_mul_f32 v[4:5], v[92:93], v[104:105] op_sel_hi:[1,0]
	v_pk_mul_f32 v[44:45], v[92:93], v[104:105] op_sel:[0,1]
	v_pk_mul_f32 v[60:61], v[92:93], v[106:107] op_sel_hi:[1,0]
	v_pk_add_f32 v[100:101], v[92:93], v[46:47]
	v_pk_fma_f32 v[4:5], v[46:47], v[12:13], v[4:5] op_sel_hi:[1,0,1]
	v_pk_fma_f32 v[44:45], v[46:47], v[12:13], v[44:45] op_sel:[0,1,0]
	v_pk_fma_f32 v[60:61], v[46:47], v[14:15], v[60:61] op_sel_hi:[1,0,1]
	v_pk_add_f32 v[100:101], v[100:101], v[62:63]
	v_pk_fma_f32 v[4:5], v[62:63], v[80:81], v[4:5] op_sel_hi:[1,0,1]
	v_pk_fma_f32 v[44:45], v[62:63], v[80:81], v[44:45] op_sel:[0,1,0]
	v_pk_fma_f32 v[60:61], v[62:63], v[82:83], v[60:61] op_sel_hi:[1,0,1]
	s_waitcnt lgkmcnt(0)
	s_barrier
	s_add_i32 s5, s34, 5
	s_min_i32 s5, s5, 0x200
	s_mul_i32 s6, s5, 0x804
	s_add_i32 s6, s6, s35
	s_add_i32 s7, s6, 0x505014
	s_add_i32 s8, s6, 0x606018
	s_mul_i32 s9, s5, 0x180c
	s_add_i32 s9, s9, s33
	s_add_i32 s4, s34, 6
	s_min_i32 s4, s4, 0x200
	s_mul_i32 s4, s4, 0x804
	s_add_i32 s4, s4, s38
	buffer_load_dword v16, v28, s[20:23], s4 offen nt
	buffer_load_dwordx3 v[168:170], v27, s[24:27], s9 offen nt
	buffer_load_dword v46, v28, s[16:19], s7 offen nt
	buffer_load_dword v47, v28, s[16:19], s8 offen nt
	v_pk_add_f32 v[62:63], v[122:123], v[100:101]
	v_pk_add_f32 v[116:117], v[152:153], v[62:63]
	v_pk_add_f32 v[122:123], v[38:39], v[4:5]
	v_pk_add_f32 v[142:143], v[140:141], v[122:123]
	v_pk_add_f32 v[38:39], v[50:51], v[44:45]
	v_pk_add_f32 v[146:147], v[144:145], v[38:39]
	v_pk_add_f32 v[50:51], v[102:103], v[60:61]
	v_pk_add_f32 v[150:151], v[148:149], v[50:51]
	v_pk_fma_f32 v[142:143], v[132:133], v[116:117], v[142:143] op_sel_hi:[0,1,1] neg_lo:[1,0,0] neg_hi:[1,0,0]
	v_pk_fma_f32 v[146:147], v[132:133], v[116:117], v[146:147] op_sel:[1,0,0] neg_lo:[1,0,0] neg_hi:[1,0,0]
	v_pk_fma_f32 v[150:151], v[134:135], v[116:117], v[150:151] op_sel_hi:[0,1,1] neg_lo:[1,0,0] neg_hi:[1,0,0]
	v_pk_mul_f32 v[120:121], v[134:135], v[142:143] op_sel:[1,0]
	v_pk_mul_f32 v[124:125], v[160:161], v[142:143] op_sel_hi:[0,1]
	v_pk_mul_f32 v[128:129], v[160:161], v[142:143] op_sel:[1,0]
	v_pk_fma_f32 v[120:121], v[160:161], v[146:147], v[120:121] op_sel_hi:[0,1,1]
	v_pk_fma_f32 v[124:125], v[162:163], v[146:147], v[124:125] op_sel_hi:[0,1,1]
	v_pk_fma_f32 v[128:129], v[162:163], v[146:147], v[128:129] op_sel:[1,0,0]
	v_pk_fma_f32 v[120:121], v[160:161], v[150:151], v[120:121] op_sel:[1,0,0]
	v_pk_fma_f32 v[124:125], v[162:163], v[150:151], v[124:125] op_sel:[1,0,0]
	v_pk_fma_f32 v[128:129], v[164:165], v[150:151], v[128:129] op_sel_hi:[0,1,1]
	v_pk_mul_f32 v[102:103], v[132:133], v[120:121] op_sel_hi:[0,1]
	v_pk_fma_f32 v[102:103], v[132:133], v[124:125], v[102:103] op_sel:[1,0,0]
	v_pk_fma_f32 v[102:103], v[134:135], v[128:129], v[102:103] op_sel_hi:[0,1,1]
	v_pk_fma_f32 v[102:103], v[164:165], v[116:117], v[102:103] op_sel:[1,0,0] neg_lo:[0,0,1] neg_hi:[0,0,1]
	v_cmp_eq_u32_e64 s[10:11], 6, v167
	v_cmp_eq_u32_e64 s[14:15], 7, v167
	v_pk_add_f32 v[116:117], v[52:53], v[120:121]
	v_pk_add_f32 v[140:141], v[90:91], v[116:117]
	v_pk_add_f32 v[52:53], v[64:65], v[124:125]
	v_pk_add_f32 v[90:91], v[94:95], v[52:53]
	v_pk_add_f32 v[64:65], v[72:73], v[128:129]
	v_pk_add_f32 v[94:95], v[98:99], v[64:65]
	v_pk_add_f32 v[98:99], v[74:75], v[102:103]
	v_pk_add_f32 v[72:73], v[68:69], v[98:99]
	v_pk_fma_f32 v[68:69], v[108:109], v[140:141], v[72:73] op_sel_hi:[0,1,1]
	v_pk_fma_f32 v[144:145], v[112:113], v[140:141], v[72:73] op_sel_hi:[0,1,1]
	v_pk_fma_f32 v[68:69], v[108:109], v[90:91], v[68:69] op_sel:[1,0,0]
	v_pk_fma_f32 v[144:145], v[112:113], v[90:91], v[144:145] op_sel:[1,0,0]
	v_pk_fma_f32 v[68:69], v[110:111], v[94:95], v[68:69] op_sel_hi:[0,1,1]
	v_pk_fma_f32 v[144:145], v[114:115], v[94:95], v[144:145] op_sel_hi:[0,1,1]
	v_pk_fma_f32 v[72:73], v[32:33], v[140:141], v[72:73] op_sel_hi:[0,1,1]
	v_pk_fma_f32 v[72:73], v[32:33], v[90:91], v[72:73] op_sel:[1,0,0]
	v_pk_fma_f32 v[72:73], v[34:35], v[94:95], v[72:73] op_sel_hi:[0,1,1]
	v_cndmask_b32_e64 v74, 0, v18, s[10:11]
	v_cndmask_b32_e64 v75, 0, v18, s[14:15]
	v_add_f32_dpp v72, v68, v72 wave_shl:1 row_mask:0xf bank_mask:0xf bound_ctrl:1
	v_add_f32_dpp v73, v69, v73 wave_shl:1 row_mask:0xf bank_mask:0xf bound_ctrl:1
	s_add_i32 s4, s34, 0
	s_cmpk_lt_i32 s4, 0x201
	s_cselect_b64 s[12:13], s[0:1], 0
	v_add_f32_dpp v72, v144, v72 wave_shr:1 row_mask:0xf bank_mask:0xf bound_ctrl:1
	v_add_f32_dpp v73, v145, v73 wave_shr:1 row_mask:0xf bank_mask:0xf bound_ctrl:1
	v_pk_fma_f32 v[72:73], v[20:21], v[166:167], v[72:73] op_sel_hi:[1,0,1] neg_lo:[0,0,1] neg_hi:[0,0,1]
	v_pk_add_f32 v[72:73], v[72:73], v[74:75] neg_lo:[0,1] neg_hi:[0,1]
	v_pk_mul_f32 v[142:143], v[72:73], v[72:73]
	v_add_f32_e32 v142, v142, v143
	v_cndmask_b32_e64 v143, 0, v142, s[12:13]
	v_add_f32_e32 v1, v1, v143
	s_waitcnt vmcnt(8)
	v_mov_b32_dpp v32, v156 wave_shr:1 row_mask:0xf bank_mask:0xf bound_ctrl:1
	v_mov_b32_dpp v33, v157 wave_shr:1 row_mask:0xf bank_mask:0xf bound_ctrl:1
	v_mov_b32_dpp v34, v158 wave_shr:1 row_mask:0xf bank_mask:0xf bound_ctrl:1
	v_mov_b32_dpp v72, v156 wave_shl:1 row_mask:0xf bank_mask:0xf bound_ctrl:1
	v_mov_b32_dpp v73, v157 wave_shl:1 row_mask:0xf bank_mask:0xf bound_ctrl:1
	v_mov_b32_dpp v74, v158 wave_shl:1 row_mask:0xf bank_mask:0xf bound_ctrl:1
	s_add_i32 s4, s34, 4
	s_cmpk_lt_u32 s4, 0x201
	s_cselect_b64 s[12:13], s[40:41], 0
	v_cmp_eq_u32_e64 s[14:15], s37, v2
	s_and_b64 s[14:15], s[14:15], s[12:13]
	v_cndmask_b32_e64 v29, 0, 1, s[14:15]
	v_pk_add_f32 v[20:21], v[156:157], v[32:33]
	v_pk_mul_f32 v[68:69], v[156:157], v[156:157] op_sel_hi:[0,1]
	v_or_b32_dpp v56, v29, v29 wave_shr:1 row_mask:0xf bank_mask:0xf bound_ctrl:1
	v_pk_mul_f32 v[90:91], v[156:157], v[158:159] op_sel_hi:[1,0]
	v_or_b32_dpp v56, v29, v56 wave_shl:1 row_mask:0xf bank_mask:0xf bound_ctrl:1
	v_mul_f32_e64 v94, v157, v157
	v_mul_f32_e64 v95, v158, v158
	v_or_b32_dpp v84, v56, v56 wave_shr:1 row_mask:0xf bank_mask:0xf bound_ctrl:1
	v_add_f32_e64 v108, v158, v34
	v_pk_add_f32 v[20:21], v[20:21], v[72:73]
	v_or_b32_dpp v84, v56, v84 wave_shl:1 row_mask:0xf bank_mask:0xf bound_ctrl:1
	v_or3_b32 v29, v84, v85, v57
	v_or3_b32 v29, v29, v88, v89
	s_add_i32 s4, s34, 1
	s_cmpk_lt_u32 s4, 0x1ff
	s_cselect_b64 s[12:13], s[42:43], 0
	v_cmp_ne_u32_e64 s[30:31], 0, v29
	s_and_b64 s[30:31], s[30:31], s[12:13]
	v_cndmask_b32_e64 v29, 0, 1.0, s[30:31]
	v_pk_fma_f32 v[68:69], v[32:33], v[32:33], v[68:69] op_sel_hi:[0,1,1]
	v_pk_fma_f32 v[90:91], v[32:33], v[34:35], v[90:91] op_sel_hi:[1,0,1]
	v_fma_f32 v94, v33, v33, v94
	v_fma_f32 v95, v34, v34, v95
	v_add_f32_dpp v109, v29, v29 wave_shr:1 row_mask:0xf bank_mask:0xf bound_ctrl:1
	v_add_f32_e64 v108, v108, v74
	v_pk_fma_f32 v[68:69], v[72:73], v[72:73], v[68:69] op_sel_hi:[0,1,1]
	v_pk_fma_f32 v[90:91], v[72:73], v[74:75], v[90:91] op_sel_hi:[1,0,1]
	v_fma_f32 v94, v73, v73, v94
	v_fma_f32 v95, v74, v74, v95
	v_add_f32_dpp v109, v29, v109 wave_shl:1 row_mask:0xf bank_mask:0xf bound_ctrl:1
	v_pk_add_f32 v[110:111], v[86:87], v[20:21]
	v_pk_add_f32 v[86:87], v[126:127], v[68:69]
	v_pk_add_f32 v[112:113], v[130:131], v[90:91]
	v_pk_add_f32 v[114:115], v[96:97], v[94:95]
	v_pk_add_f32 v[96:97], v[118:119], v[108:109]
	v_mul_f32_e64 v132, v110, v22
	v_mul_f32_e64 v133, v111, v22
	v_mul_f32_e64 v134, v96, v22
	v_fma_f32 v29, v86, v22, v26
	v_mul_f32_e64 v56, v87, v22
	v_mul_f32_e64 v118, v112, v22
	v_fma_f32 v119, v114, v22, v26
	v_mul_f32_e64 v126, v113, v22
	v_fma_f32 v127, v115, v22, v26
	v_fma_f32 v29, -v132, v132, v29
	v_fma_f32 v56, -v132, v133, v56
	v_fma_f32 v118, -v132, v134, v118
	v_fma_f32 v119, -v133, v133, v119
	v_fma_f32 v126, -v133, v134, v126
	v_fma_f32 v127, -v134, v134, v127
	v_mul_f32_e64 v130, v126, v126
	v_mul_f32_e64 v131, v56, v127
	v_mul_f32_e64 v148, v118, v119
	v_mul_f32_e64 v149, v118, v118
	v_mul_f32_e64 v150, v29, v126
	v_mul_f32_e64 v151, v56, v56
	v_fma_f32 v130, v119, v127, -v130
	v_fma_f32 v131, v118, v126, -v131
	v_fma_f32 v148, v56, v126, -v148
	v_fma_f32 v149, v29, v127, -v149
	v_fma_f32 v150, v56, v118, -v150
	v_fma_f32 v151, v29, v119, -v151
	v_mul_f32_e64 v152, v29, v130
	v_fma_f32 v152, v56, v131, v152
	v_fma_f32 v152, v118, v148, v152
	v_rcp_f32_e32 v152, v152
	v_cmp_ne_u32_e64 vcc, s37, v17
	v_mul_f32_e64 v152, v152, v22
	v_cndmask_b32_e64 v152, 0, v152, s[30:31]
	v_cndmask_b32_e64 v29, 0, v18, vcc
	v_cndmask_b32_e64 v145, 0, v22, s[30:31]
	v_mul_f32_e64 v135, v130, v152
	v_mul_f32_e64 v140, v131, v152
	v_mul_f32_e64 v141, v148, v152
	v_mul_f32_e64 v142, v149, v152
	v_mul_f32_e64 v143, v150, v152
	v_mul_f32_e64 v144, v151, v152
	v_add_f32_e64 v146, v97, v29
	v_mov_b32_e32 v147, v17
	ds_write_b128 v23, v[132:135] offset:3072
	ds_write_b128 v23, v[140:143] offset:4096
	ds_write_b128 v23, v[144:147] offset:5120
	v_mov_b32_dpp v96, v54 wave_shr:1 row_mask:0xf bank_mask:0xf bound_ctrl:1
	v_mov_b32_dpp v97, v55 wave_shr:1 row_mask:0xf bank_mask:0xf bound_ctrl:1
	v_mov_b32_dpp v112, v54 wave_shl:1 row_mask:0xf bank_mask:0xf bound_ctrl:1
	v_mov_b32_dpp v113, v55 wave_shl:1 row_mask:0xf bank_mask:0xf bound_ctrl:1
	v_pk_mul_f32 v[86:87], v[54:55], v[156:157] op_sel_hi:[1,0]
	v_pk_mul_f32 v[110:111], v[54:55], v[156:157] op_sel:[0,1]
	v_pk_mul_f32 v[114:115], v[54:55], v[158:159] op_sel_hi:[1,0]
	v_pk_add_f32 v[118:119], v[54:55], v[96:97]
	v_pk_fma_f32 v[86:87], v[96:97], v[32:33], v[86:87] op_sel_hi:[1,0,1]
	v_pk_fma_f32 v[110:111], v[96:97], v[32:33], v[110:111] op_sel:[0,1,0]
	v_pk_fma_f32 v[114:115], v[96:97], v[34:35], v[114:115] op_sel_hi:[1,0,1]
	v_pk_add_f32 v[118:119], v[118:119], v[112:113]
	v_pk_fma_f32 v[86:87], v[112:113], v[72:73], v[86:87] op_sel_hi:[1,0,1]
	v_pk_fma_f32 v[110:111], v[112:113], v[72:73], v[110:111] op_sel:[0,1,0]
	v_pk_fma_f32 v[114:115], v[112:113], v[74:75], v[114:115] op_sel_hi:[1,0,1]
	s_waitcnt lgkmcnt(0)
	s_barrier
	s_add_i32 s5, s34, 6
	s_min_i32 s5, s5, 0x200
	s_mul_i32 s6, s5, 0x804
	s_add_i32 s6, s6, s35
	s_add_i32 s7, s6, 0x505014
	s_add_i32 s8, s6, 0x606018
	s_mul_i32 s9, s5, 0x180c
	s_add_i32 s9, s9, s33
	s_add_i32 s4, s34, 7
	s_min_i32 s4, s4, 0x200
	s_mul_i32 s4, s4, 0x804
	s_add_i32 s4, s4, s38
	buffer_load_dword v17, v28, s[20:23], s4 offen nt
	buffer_load_dwordx3 v[148:150], v27, s[24:27], s9 offen nt
	buffer_load_dword v96, v28, s[16:19], s7 offen nt
	buffer_load_dword v97, v28, s[16:19], s8 offen nt
	v_pk_add_f32 v[112:113], v[62:63], v[118:119]
	v_pk_add_f32 v[62:63], v[122:123], v[86:87]
	v_pk_add_f32 v[122:123], v[38:39], v[110:111]
	v_pk_add_f32 v[38:39], v[50:51], v[114:115]
	v_pk_fma_f32 v[62:63], v[132:133], v[112:113], v[62:63] op_sel_hi:[0,1,1] neg_lo:[1,0,0] neg_hi:[1,0,0]
	v_pk_fma_f32 v[122:123], v[132:133], v[112:113], v[122:123] op_sel:[1,0,0] neg_lo:[1,0,0] neg_hi:[1,0,0]
	v_pk_fma_f32 v[38:39], v[134:135], v[112:113], v[38:39] op_sel_hi:[0,1,1] neg_lo:[1,0,0] neg_hi:[1,0,0]
	v_pk_mul_f32 v[152:153], v[134:135], v[62:63] op_sel:[1,0]
	v_pk_mul_f32 v[160:161], v[140:141], v[62:63] op_sel_hi:[0,1]
	v_pk_mul_f32 v[164:165], v[140:141], v[62:63] op_sel:[1,0]
	v_pk_fma_f32 v[152:153], v[140:141], v[122:123], v[152:153] op_sel_hi:[0,1,1]
	v_pk_fma_f32 v[160:161], v[142:143], v[122:123], v[160:161] op_sel_hi:[0,1,1]
	v_pk_fma_f32 v[164:165], v[142:143], v[122:123], v[164:165] op_sel:[1,0,0]
	v_pk_fma_f32 v[152:153], v[140:141], v[38:39], v[152:153] op_sel:[1,0,0]
	v_pk_fma_f32 v[160:161], v[142:143], v[38:39], v[160:161] op_sel:[1,0,0]
	v_pk_fma_f32 v[164:165], v[144:145], v[38:39], v[164:165] op_sel_hi:[0,1,1]
	v_pk_mul_f32 v[50:51], v[132:133], v[152:153] op_sel_hi:[0,1]
	v_pk_fma_f32 v[50:51], v[132:133], v[160:161], v[50:51] op_sel:[1,0,0]
	v_pk_fma_f32 v[50:51], v[134:135], v[164:165], v[50:51] op_sel_hi:[0,1,1]
	v_pk_fma_f32 v[50:51], v[144:145], v[112:113], v[50:51] op_sel:[1,0,0] neg_lo:[0,0,1] neg_hi:[0,0,1]
	v_cmp_eq_u32_e64 s[10:11], 6, v147
	v_cmp_eq_u32_e64 s[14:15], 7, v147
	v_pk_add_f32 v[38:39], v[116:117], v[152:153]
	v_pk_add_f32 v[62:63], v[52:53], v[160:161]
	v_pk_add_f32 v[52:53], v[64:65], v[164:165]
	v_pk_add_f32 v[64:65], v[98:99], v[50:51]
	v_pk_fma_f32 v[112:113], v[8:9], v[38:39], v[64:65] op_sel_hi:[0,1,1]
	v_pk_fma_f32 v[116:117], v[40:41], v[38:39], v[64:65] op_sel_hi:[0,1,1]
	v_pk_fma_f32 v[112:113], v[8:9], v[62:63], v[112:113] op_sel:[1,0,0]
	v_pk_fma_f32 v[116:117], v[40:41], v[62:63], v[116:117] op_sel:[1,0,0]
	v_pk_fma_f32 v[112:113], v[10:11], v[52:53], v[112:113] op_sel_hi:[0,1,1]
	v_pk_fma_f32 v[116:117], v[42:43], v[52:53], v[116:117] op_sel_hi:[0,1,1]
	v_pk_fma_f32 v[64:65], v[76:77], v[38:39], v[64:65] op_sel_hi:[0,1,1]
	v_pk_fma_f32 v[64:65], v[76:77], v[62:63], v[64:65] op_sel:[1,0,0]
	v_pk_fma_f32 v[64:65], v[78:79], v[52:53], v[64:65] op_sel_hi:[0,1,1]
	v_cndmask_b32_e64 v98, 0, v18, s[10:11]
	v_cndmask_b32_e64 v99, 0, v18, s[14:15]
	v_add_f32_dpp v64, v112, v64 wave_shl:1 row_mask:0xf bank_mask:0xf bound_ctrl:1
	v_add_f32_dpp v65, v113, v65 wave_shl:1 row_mask:0xf bank_mask:0xf bound_ctrl:1
	s_add_i32 s4, s34, 1
	s_cmpk_lt_i32 s4, 0x201
	s_cselect_b64 s[12:13], s[0:1], 0
	v_add_f32_dpp v64, v116, v64 wave_shr:1 row_mask:0xf bank_mask:0xf bound_ctrl:1
	v_add_f32_dpp v65, v117, v65 wave_shr:1 row_mask:0xf bank_mask:0xf bound_ctrl:1
	v_pk_fma_f32 v[64:65], v[30:31], v[146:147], v[64:65] op_sel_hi:[1,0,1] neg_lo:[0,0,1] neg_hi:[0,0,1]
	v_pk_add_f32 v[64:65], v[64:65], v[98:99] neg_lo:[0,1] neg_hi:[0,1]
	v_pk_mul_f32 v[122:123], v[64:65], v[64:65]
	v_add_f32_e32 v122, v122, v123
	v_cndmask_b32_e64 v123, 0, v122, s[12:13]
	v_add_f32_e32 v1, v1, v123
	s_waitcnt vmcnt(8)
	v_mov_b32_dpp v8, v136 wave_shr:1 row_mask:0xf bank_mask:0xf bound_ctrl:1
	v_mov_b32_dpp v9, v137 wave_shr:1 row_mask:0xf bank_mask:0xf bound_ctrl:1
	v_mov_b32_dpp v10, v138 wave_shr:1 row_mask:0xf bank_mask:0xf bound_ctrl:1
	v_mov_b32_dpp v40, v136 wave_shl:1 row_mask:0xf bank_mask:0xf bound_ctrl:1
	v_mov_b32_dpp v41, v137 wave_shl:1 row_mask:0xf bank_mask:0xf bound_ctrl:1
	v_mov_b32_dpp v42, v138 wave_shl:1 row_mask:0xf bank_mask:0xf bound_ctrl:1
	s_add_i32 s4, s34, 5
	s_cmpk_lt_u32 s4, 0x201
	s_cselect_b64 s[12:13], s[40:41], 0
	v_cmp_eq_u32_e64 s[14:15], s37, v3
	s_and_b64 s[14:15], s[14:15], s[12:13]
	v_cndmask_b32_e64 v29, 0, 1, s[14:15]
	v_pk_add_f32 v[30:31], v[136:137], v[8:9]
	v_pk_mul_f32 v[38:39], v[136:137], v[136:137] op_sel_hi:[0,1]
	v_or_b32_dpp v56, v29, v29 wave_shr:1 row_mask:0xf bank_mask:0xf bound_ctrl:1
	v_pk_mul_f32 v[52:53], v[136:137], v[138:139] op_sel_hi:[1,0]
	v_or_b32_dpp v56, v29, v56 wave_shl:1 row_mask:0xf bank_mask:0xf bound_ctrl:1
	v_mul_f32_e64 v62, v137, v137
	v_mul_f32_e64 v63, v138, v138
	v_or_b32_dpp v89, v56, v56 wave_shr:1 row_mask:0xf bank_mask:0xf bound_ctrl:1
	v_add_f32_e64 v64, v138, v10
	v_pk_add_f32 v[30:31], v[30:31], v[40:41]
	v_or_b32_dpp v89, v56, v89 wave_shl:1 row_mask:0xf bank_mask:0xf bound_ctrl:1
	v_or3_b32 v29, v89, v84, v85
	v_or3_b32 v29, v29, v57, v88
	s_add_i32 s4, s34, 2
	s_cmpk_lt_u32 s4, 0x1ff
	s_cselect_b64 s[12:13], s[42:43], 0
	v_cmp_ne_u32_e64 s[30:31], 0, v29
	s_and_b64 s[30:31], s[30:31], s[12:13]
	v_cndmask_b32_e64 v29, 0, 1.0, s[30:31]
	v_pk_fma_f32 v[38:39], v[8:9], v[8:9], v[38:39] op_sel_hi:[0,1,1]
	v_pk_fma_f32 v[52:53], v[8:9], v[10:11], v[52:53] op_sel_hi:[1,0,1]
	v_fma_f32 v62, v9, v9, v62
	v_fma_f32 v63, v10, v10, v63
	v_add_f32_dpp v65, v29, v29 wave_shr:1 row_mask:0xf bank_mask:0xf bound_ctrl:1
	v_add_f32_e64 v64, v64, v42
	v_pk_fma_f32 v[38:39], v[40:41], v[40:41], v[38:39] op_sel_hi:[0,1,1]
	v_pk_fma_f32 v[52:53], v[40:41], v[42:43], v[52:53] op_sel_hi:[1,0,1]
	v_fma_f32 v62, v41, v41, v62
	v_fma_f32 v63, v42, v42, v63
	v_add_f32_dpp v65, v29, v65 wave_shl:1 row_mask:0xf bank_mask:0xf bound_ctrl:1
	v_pk_add_f32 v[76:77], v[20:21], v[30:31]
	v_pk_add_f32 v[78:79], v[6:7], v[76:77]
	v_pk_add_f32 v[6:7], v[68:69], v[38:39]
	v_pk_add_f32 v[20:21], v[48:49], v[6:7]
	v_pk_add_f32 v[48:49], v[90:91], v[52:53]
	v_pk_add_f32 v[68:69], v[58:59], v[48:49]
	v_pk_add_f32 v[112:113], v[94:95], v[62:63]
	v_pk_add_f32 v[58:59], v[66:67], v[112:113]
	v_pk_add_f32 v[116:117], v[108:109], v[64:65]
	v_pk_add_f32 v[66:67], v[70:71], v[116:117]
	v_mul_f32_e64 v132, v78, v22
	v_mul_f32_e64 v133, v79, v22
	v_mul_f32_e64 v134, v66, v22
	v_fma_f32 v29, v20, v22, v26
	v_mul_f32_e64 v56, v21, v22
	v_mul_f32_e64 v70, v68, v22
	v_fma_f32 v71, v58, v22, v26
	v_mul_f32_e64 v90, v69, v22
	v_fma_f32 v91, v59, v22, v26
	v_fma_f32 v29, -v132, v132, v29
	v_fma_f32 v56, -v132, v133, v56
	v_fma_f32 v70, -v132, v134, v70
	v_fma_f32 v71, -v133, v133, v71
	v_fma_f32 v90, -v133, v134, v90
	v_fma_f32 v91, -v134, v134, v91
	v_mul_f32_e64 v94, v90, v90
	v_mul_f32_e64 v95, v56, v91
	v_mul_f32_e64 v98, v70, v71
	v_mul_f32_e64 v99, v70, v70
	v_mul_f32_e64 v108, v29, v90
	v_mul_f32_e64 v109, v56, v56
	v_fma_f32 v94, v71, v91, -v94
	v_fma_f32 v95, v70, v90, -v95
	v_fma_f32 v98, v56, v90, -v98
	v_fma_f32 v99, v29, v91, -v99
	v_fma_f32 v108, v56, v70, -v108
	v_fma_f32 v109, v29, v71, -v109
	v_mul_f32_e64 v122, v29, v94
	v_fma_f32 v122, v56, v95, v122
	v_fma_f32 v122, v70, v98, v122
	v_rcp_f32_e32 v122, v122
	v_cmp_ne_u32_e64 vcc, s37, v25
	v_mul_f32_e64 v122, v122, v22
	v_cndmask_b32_e64 v122, 0, v122, s[30:31]
	v_cndmask_b32_e64 v29, 0, v18, vcc
	v_cndmask_b32_e64 v145, 0, v22, s[30:31]
	v_mul_f32_e64 v135, v94, v122
	v_mul_f32_e64 v140, v95, v122
	v_mul_f32_e64 v141, v98, v122
	v_mul_f32_e64 v142, v99, v122
	v_mul_f32_e64 v143, v108, v122
	v_mul_f32_e64 v144, v109, v122
	v_add_f32_e64 v146, v67, v29
	v_mov_b32_e32 v147, v25
	ds_write_b128 v23, v[132:135]
	ds_write_b128 v23, v[140:143] offset:1024
	ds_write_b128 v23, v[144:147] offset:2048
	v_mov_b32_dpp v58, v36 wave_shr:1 row_mask:0xf bank_mask:0xf bound_ctrl:1
	v_mov_b32_dpp v59, v37 wave_shr:1 row_mask:0xf bank_mask:0xf bound_ctrl:1
	v_mov_b32_dpp v66, v36 wave_shl:1 row_mask:0xf bank_mask:0xf bound_ctrl:1
	v_mov_b32_dpp v67, v37 wave_shl:1 row_mask:0xf bank_mask:0xf bound_ctrl:1
	v_pk_mul_f32 v[20:21], v[36:37], v[136:137] op_sel_hi:[1,0]
	v_pk_mul_f32 v[68:69], v[36:37], v[136:137] op_sel:[0,1]
	v_pk_mul_f32 v[108:109], v[36:37], v[138:139] op_sel_hi:[1,0]
	v_pk_add_f32 v[172:173], v[36:37], v[58:59]
	v_pk_fma_f32 v[20:21], v[58:59], v[8:9], v[20:21] op_sel_hi:[1,0,1]
	v_pk_fma_f32 v[68:69], v[58:59], v[8:9], v[68:69] op_sel:[0,1,0]
	v_pk_fma_f32 v[108:109], v[58:59], v[10:11], v[108:109] op_sel_hi:[1,0,1]
	v_pk_add_f32 v[172:173], v[172:173], v[66:67]
	v_pk_fma_f32 v[20:21], v[66:67], v[40:41], v[20:21] op_sel_hi:[1,0,1]
	v_pk_fma_f32 v[68:69], v[66:67], v[40:41], v[68:69] op_sel:[0,1,0]
	v_pk_fma_f32 v[108:109], v[66:67], v[42:43], v[108:109] op_sel_hi:[1,0,1]
	s_waitcnt lgkmcnt(0)
	s_barrier
	s_add_i32 s5, s34, 7
	s_min_i32 s5, s5, 0x200
	s_mul_i32 s6, s5, 0x804
	s_add_i32 s6, s6, s35
	s_add_i32 s7, s6, 0x505014
	s_add_i32 s8, s6, 0x606018
	s_mul_i32 s9, s5, 0x180c
	s_add_i32 s9, s9, s33
	s_add_i32 s4, s34, 8
	s_min_i32 s4, s4, 0x200
	s_mul_i32 s4, s4, 0x804
	s_add_i32 s4, s4, s38
	buffer_load_dword v25, v28, s[20:23], s4 offen nt
	buffer_load_dwordx3 v[176:178], v27, s[24:27], s9 offen nt
	buffer_load_dword v58, v28, s[16:19], s7 offen nt
	buffer_load_dword v59, v28, s[16:19], s8 offen nt
	v_pk_add_f32 v[66:67], v[118:119], v[172:173]
	v_pk_add_f32 v[70:71], v[100:101], v[66:67]
	v_pk_add_f32 v[78:79], v[86:87], v[20:21]
	v_pk_add_f32 v[100:101], v[4:5], v[78:79]
	v_pk_add_f32 v[86:87], v[110:111], v[68:69]
	v_pk_add_f32 v[4:5], v[44:45], v[86:87]
	v_pk_add_f32 v[90:91], v[114:115], v[108:109]
	v_pk_add_f32 v[44:45], v[60:61], v[90:91]
	v_pk_fma_f32 v[100:101], v[132:133], v[70:71], v[100:101] op_sel_hi:[0,1,1] neg_lo:[1,0,0] neg_hi:[1,0,0]
	v_pk_fma_f32 v[4:5], v[132:133], v[70:71], v[4:5] op_sel:[1,0,0] neg_lo:[1,0,0] neg_hi:[1,0,0]
	v_pk_fma_f32 v[44:45], v[134:135], v[70:71], v[44:45] op_sel_hi:[0,1,1] neg_lo:[1,0,0] neg_hi:[1,0,0]
	v_pk_mul_f32 v[94:95], v[134:135], v[100:101] op_sel:[1,0]
	v_pk_mul_f32 v[98:99], v[140:141], v[100:101] op_sel_hi:[0,1]
	v_pk_mul_f32 v[110:111], v[140:141], v[100:101] op_sel:[1,0]
	v_pk_fma_f32 v[94:95], v[140:141], v[4:5], v[94:95] op_sel_hi:[0,1,1]
	v_pk_fma_f32 v[98:99], v[142:143], v[4:5], v[98:99] op_sel_hi:[0,1,1]
	v_pk_fma_f32 v[110:111], v[142:143], v[4:5], v[110:111] op_sel:[1,0,0]
	v_pk_fma_f32 v[94:95], v[140:141], v[44:45], v[94:95] op_sel:[1,0,0]
	v_pk_fma_f32 v[98:99], v[142:143], v[44:45], v[98:99] op_sel:[1,0,0]
	v_pk_fma_f32 v[110:111], v[144:145], v[44:45], v[110:111] op_sel_hi:[0,1,1]
	v_pk_mul_f32 v[60:61], v[132:133], v[94:95] op_sel_hi:[0,1]
	v_pk_fma_f32 v[60:61], v[132:133], v[98:99], v[60:61] op_sel:[1,0,0]
	v_pk_fma_f32 v[60:61], v[134:135], v[110:111], v[60:61] op_sel_hi:[0,1,1]
	v_pk_fma_f32 v[60:61], v[144:145], v[70:71], v[60:61] op_sel:[1,0,0] neg_lo:[0,0,1] neg_hi:[0,0,1]
	v_cmp_eq_u32_e64 s[10:11], 6, v147
	v_cmp_eq_u32_e64 s[14:15], 7, v147
	v_pk_add_f32 v[70:71], v[152:153], v[94:95]
	v_pk_add_f32 v[4:5], v[120:121], v[70:71]
	v_pk_add_f32 v[114:115], v[160:161], v[98:99]
	v_pk_add_f32 v[44:45], v[124:125], v[114:115]
	v_pk_add_f32 v[118:119], v[164:165], v[110:111]
	v_pk_add_f32 v[100:101], v[128:129], v[118:119]
	v_pk_add_f32 v[120:121], v[50:51], v[60:61]
	v_pk_add_f32 v[122:123], v[102:103], v[120:121]
	v_pk_fma_f32 v[50:51], v[12:13], v[4:5], v[122:123] op_sel_hi:[0,1,1]
	v_pk_fma_f32 v[102:103], v[80:81], v[4:5], v[122:123] op_sel_hi:[0,1,1]
	v_pk_fma_f32 v[50:51], v[12:13], v[44:45], v[50:51] op_sel:[1,0,0]
	v_pk_fma_f32 v[102:103], v[80:81], v[44:45], v[102:103] op_sel:[1,0,0]
	v_pk_fma_f32 v[50:51], v[14:15], v[100:101], v[50:51] op_sel_hi:[0,1,1]
	v_pk_fma_f32 v[102:103], v[82:83], v[100:101], v[102:103] op_sel_hi:[0,1,1]
	v_pk_fma_f32 v[122:123], v[104:105], v[4:5], v[122:123] op_sel_hi:[0,1,1]
	v_pk_fma_f32 v[122:123], v[104:105], v[44:45], v[122:123] op_sel:[1,0,0]
	v_pk_fma_f32 v[122:123], v[106:107], v[100:101], v[122:123] op_sel_hi:[0,1,1]
	v_cndmask_b32_e64 v124, 0, v18, s[10:11]
	v_cndmask_b32_e64 v125, 0, v18, s[14:15]
	v_add_f32_dpp v122, v50, v122 wave_shl:1 row_mask:0xf bank_mask:0xf bound_ctrl:1
	v_add_f32_dpp v123, v51, v123 wave_shl:1 row_mask:0xf bank_mask:0xf bound_ctrl:1
	s_add_i32 s4, s34, 2
	s_cmpk_lt_i32 s4, 0x201
	s_cselect_b64 s[12:13], s[0:1], 0
	v_add_f32_dpp v122, v102, v122 wave_shr:1 row_mask:0xf bank_mask:0xf bound_ctrl:1
	v_add_f32_dpp v123, v103, v123 wave_shr:1 row_mask:0xf bank_mask:0xf bound_ctrl:1
	v_pk_fma_f32 v[122:123], v[92:93], v[146:147], v[122:123] op_sel_hi:[1,0,1] neg_lo:[0,0,1] neg_hi:[0,0,1]
	v_pk_add_f32 v[122:123], v[122:123], v[124:125] neg_lo:[0,1] neg_hi:[0,1]
	v_pk_mul_f32 v[126:127], v[122:123], v[122:123]
	v_add_f32_e32 v126, v126, v127
	v_cndmask_b32_e64 v127, 0, v126, s[12:13]
	v_add_f32_e32 v1, v1, v127
	s_waitcnt vmcnt(8)
	v_mov_b32_dpp v12, v168 wave_shr:1 row_mask:0xf bank_mask:0xf bound_ctrl:1
	v_mov_b32_dpp v13, v169 wave_shr:1 row_mask:0xf bank_mask:0xf bound_ctrl:1
	v_mov_b32_dpp v14, v170 wave_shr:1 row_mask:0xf bank_mask:0xf bound_ctrl:1
	v_mov_b32_dpp v80, v168 wave_shl:1 row_mask:0xf bank_mask:0xf bound_ctrl:1
	v_mov_b32_dpp v81, v169 wave_shl:1 row_mask:0xf bank_mask:0xf bound_ctrl:1
	v_mov_b32_dpp v82, v170 wave_shl:1 row_mask:0xf bank_mask:0xf bound_ctrl:1
	s_add_i32 s4, s34, 6
	s_cmpk_lt_u32 s4, 0x201
	s_cselect_b64 s[12:13], s[40:41], 0
	v_cmp_eq_u32_e64 s[14:15], s37, v16
	s_and_b64 s[14:15], s[14:15], s[12:13]
	v_cndmask_b32_e64 v29, 0, 1, s[14:15]
	v_pk_add_f32 v[4:5], v[168:169], v[12:13]
	v_pk_mul_f32 v[44:45], v[168:169], v[168:169] op_sel_hi:[0,1]
	v_or_b32_dpp v56, v29, v29 wave_shr:1 row_mask:0xf bank_mask:0xf bound_ctrl:1
	v_pk_mul_f32 v[50:51], v[168:169], v[170:171] op_sel_hi:[1,0]
	v_or_b32_dpp v56, v29, v56 wave_shl:1 row_mask:0xf bank_mask:0xf bound_ctrl:1
	v_mul_f32_e64 v92, v169, v169
	v_mul_f32_e64 v93, v170, v170
	v_or_b32_dpp v88, v56, v56 wave_shr:1 row_mask:0xf bank_mask:0xf bound_ctrl:1
	v_add_f32_e64 v100, v170, v14
	v_pk_add_f32 v[4:5], v[4:5], v[80:81]
	v_or_b32_dpp v88, v56, v88 wave_shl:1 row_mask:0xf bank_mask:0xf bound_ctrl:1
	v_or3_b32 v29, v88, v89, v84
	v_or3_b32 v29, v29, v85, v57
	s_add_i32 s4, s34, 3
	s_cmpk_lt_u32 s4, 0x1ff
	s_cselect_b64 s[12:13], s[42:43], 0
	v_cmp_ne_u32_e64 s[30:31], 0, v29
	s_and_b64 s[30:31], s[30:31], s[12:13]
	v_cndmask_b32_e64 v29, 0, 1.0, s[30:31]
	v_pk_fma_f32 v[44:45], v[12:13], v[12:13], v[44:45] op_sel_hi:[0,1,1]
	v_pk_fma_f32 v[50:51], v[12:13], v[14:15], v[50:51] op_sel_hi:[1,0,1]
	v_fma_f32 v92, v13, v13, v92
	v_fma_f32 v93, v14, v14, v93
	v_add_f32_dpp v101, v29, v29 wave_shr:1 row_mask:0xf bank_mask:0xf bound_ctrl:1
	v_add_f32_e64 v100, v100, v82
	v_pk_fma_f32 v[44:45], v[80:81], v[80:81], v[44:45] op_sel_hi:[0,1,1]
	v_pk_fma_f32 v[50:51], v[80:81], v[82:83], v[50:51] op_sel_hi:[1,0,1]
	v_fma_f32 v92, v81, v81, v92
	v_fma_f32 v93, v82, v82, v93
	v_add_f32_dpp v101, v29, v101 wave_shl:1 row_mask:0xf bank_mask:0xf bound_ctrl:1
	v_pk_add_f32 v[102:103], v[76:77], v[4:5]
	v_pk_add_f32 v[76:77], v[6:7], v[44:45]
	v_pk_add_f32 v[6:7], v[48:49], v[50:51]
	v_pk_add_f32 v[48:49], v[112:113], v[92:93]
	v_pk_add_f32 v[104:105], v[116:117], v[100:101]
	v_mul_f32_e64 v124, v102, v22
	v_mul_f32_e64 v125, v103, v22
	v_mul_f32_e64 v126, v104, v22
	v_fma_f32 v29, v76, v22, v26
	v_mul_f32_e64 v56, v77, v22
	v_mul_f32_e64 v106, v6, v22
	v_fma_f32 v107, v48, v22, v26
	v_mul_f32_e64 v112, v7, v22
	v_fma_f32 v113, v49, v22, v26
	v_fma_f32 v29, -v124, v124, v29
	v_fma_f32 v56, -v124, v125, v56
	v_fma_f32 v106, -v124, v126, v106
	v_fma_f32 v107, -v125, v125, v107
	v_fma_f32 v112, -v125, v126, v112
	v_fma_f32 v113, -v126, v126, v113
	v_mul_f32_e64 v116, v112, v112
	v_mul_f32_e64 v117, v56, v113
	v_mul_f32_e64 v122, v106, v107
	v_mul_f32_e64 v123, v106, v106
	v_mul_f32_e64 v140, v29, v112
	v_mul_f32_e64 v141, v56, v56
	v_fma_f32 v116, v107, v113, -v116
	v_fma_f32 v117, v106, v112, -v117
	v_fma_f32 v122, v56, v112, -v122
	v_fma_f32 v123, v29, v113, -v123
	v_fma_f32 v140, v56, v106, -v140
	v_fma_f32 v141, v29, v107, -v141
	v_mul_f32_e64 v142, v29, v116
	v_fma_f32 v142, v56, v117, v142
	v_fma_f32 v142, v106, v122, v142
	v_rcp_f32_e32 v142, v142
	v_cmp_ne_u32_e64 vcc, s37, v24
	v_mul_f32_e64 v142, v142, v22
	v_cndmask_b32_e64 v142, 0, v142, s[30:31]
	v_cndmask_b32_e64 v29, 0, v18, vcc
	v_cndmask_b32_e64 v133, 0, v22, s[30:31]
	v_mul_f32_e64 v127, v116, v142
	v_mul_f32_e64 v128, v117, v142
	v_mul_f32_e64 v129, v122, v142
	v_mul_f32_e64 v130, v123, v142
	v_mul_f32_e64 v131, v140, v142
	v_mul_f32_e64 v132, v141, v142
	v_add_f32_e64 v134, v105, v29
	v_mov_b32_e32 v135, v24
	ds_write_b128 v23, v[124:127] offset:3072
	ds_write_b128 v23, v[128:131] offset:4096
	ds_write_b128 v23, v[132:135] offset:5120
	v_mov_b32_dpp v48, v46 wave_shr:1 row_mask:0xf bank_mask:0xf bound_ctrl:1
	v_mov_b32_dpp v49, v47 wave_shr:1 row_mask:0xf bank_mask:0xf bound_ctrl:1
	v_mov_b32_dpp v56, v46 wave_shl:1 row_mask:0xf bank_mask:0xf bound_ctrl:1
	v_mov_b32_dpp v57, v47 wave_shl:1 row_mask:0xf bank_mask:0xf bound_ctrl:1
	v_pk_mul_f32 v[6:7], v[46:47], v[168:169] op_sel_hi:[1,0]
	v_pk_mul_f32 v[102:103], v[46:47], v[168:169] op_sel:[0,1]
	v_pk_mul_f32 v[106:107], v[46:47], v[170:171] op_sel_hi:[1,0]
	v_pk_add_f32 v[122:123], v[46:47], v[48:49]
	v_pk_fma_f32 v[6:7], v[48:49], v[12:13], v[6:7] op_sel_hi:[1,0,1]
	v_pk_fma_f32 v[102:103], v[48:49], v[12:13], v[102:103] op_sel:[0,1,0]
	v_pk_fma_f32 v[106:107], v[48:49], v[14:15], v[106:107] op_sel_hi:[1,0,1]
	v_pk_add_f32 v[122:123], v[122:123], v[56:57]
	v_pk_fma_f32 v[6:7], v[56:57], v[80:81], v[6:7] op_sel_hi:[1,0,1]
	v_pk_fma_f32 v[102:103], v[56:57], v[80:81], v[102:103] op_sel:[0,1,0]
	v_pk_fma_f32 v[106:107], v[56:57], v[82:83], v[106:107] op_sel_hi:[1,0,1]
	s_waitcnt lgkmcnt(0)
	s_barrier
	s_add_i32 s5, s34, 8
	s_min_i32 s5, s5, 0x200
	s_mul_i32 s6, s5, 0x804
	s_add_i32 s6, s6, s35
	s_add_i32 s7, s6, 0x505014
	s_add_i32 s8, s6, 0x606018
	s_mul_i32 s9, s5, 0x180c
	s_add_i32 s9, s9, s33
	s_add_i32 s4, s34, 9
	s_min_i32 s4, s4, 0x200
	s_mul_i32 s4, s4, 0x804
	s_add_i32 s4, s4, s38
	buffer_load_dword v24, v28, s[20:23], s4 offen nt
	buffer_load_dwordx3 v[140:142], v27, s[24:27], s9 offen nt
	buffer_load_dword v48, v28, s[16:19], s7 offen nt
	buffer_load_dword v49, v28, s[16:19], s8 offen nt
	v_pk_add_f32 v[56:57], v[66:67], v[122:123]
	v_pk_add_f32 v[66:67], v[78:79], v[6:7]
	v_pk_add_f32 v[78:79], v[86:87], v[102:103]
	v_pk_add_f32 v[86:87], v[90:91], v[106:107]
	v_pk_fma_f32 v[66:67], v[124:125], v[56:57], v[66:67] op_sel_hi:[0,1,1] neg_lo:[1,0,0] neg_hi:[1,0,0]
	v_pk_fma_f32 v[78:79], v[124:125], v[56:57], v[78:79] op_sel:[1,0,0] neg_lo:[1,0,0] neg_hi:[1,0,0]
	v_pk_fma_f32 v[86:87], v[126:127], v[56:57], v[86:87] op_sel_hi:[0,1,1] neg_lo:[1,0,0] neg_hi:[1,0,0]
	v_pk_mul_f32 v[76:77], v[126:127], v[66:67] op_sel:[1,0]
	v_pk_mul_f32 v[104:105], v[128:129], v[66:67] op_sel_hi:[0,1]
	v_pk_mul_f32 v[112:113], v[128:129], v[66:67] op_sel:[1,0]
	v_pk_fma_f32 v[76:77], v[128:129], v[78:79], v[76:77] op_sel_hi:[0,1,1]
	v_pk_fma_f32 v[104:105], v[130:131], v[78:79], v[104:105] op_sel_hi:[0,1,1]
	v_pk_fma_f32 v[112:113], v[130:131], v[78:79], v[112:113] op_sel:[1,0,0]
	v_pk_fma_f32 v[76:77], v[128:129], v[86:87], v[76:77] op_sel:[1,0,0]
	v_pk_fma_f32 v[104:105], v[130:131], v[86:87], v[104:105] op_sel:[1,0,0]
	v_pk_fma_f32 v[112:113], v[132:133], v[86:87], v[112:113] op_sel_hi:[0,1,1]
	v_pk_mul_f32 v[90:91], v[124:125], v[76:77] op_sel_hi:[0,1]
	v_pk_fma_f32 v[90:91], v[124:125], v[104:105], v[90:91] op_sel:[1,0,0]
	v_pk_fma_f32 v[90:91], v[126:127], v[112:113], v[90:91] op_sel_hi:[0,1,1]
	v_pk_fma_f32 v[90:91], v[132:133], v[56:57], v[90:91] op_sel:[1,0,0] neg_lo:[0,0,1] neg_hi:[0,0,1]
	v_cmp_eq_u32_e64 s[10:11], 6, v135
	v_cmp_eq_u32_e64 s[14:15], 7, v135
	v_pk_add_f32 v[56:57], v[70:71], v[76:77]
	v_pk_add_f32 v[66:67], v[114:115], v[104:105]
	v_pk_add_f32 v[70:71], v[118:119], v[112:113]
	v_pk_add_f32 v[116:117], v[120:121], v[90:91]
	v_pk_fma_f32 v[120:121], v[32:33], v[56:57], v[116:117] op_sel_hi:[0,1,1]
	v_pk_fma_f32 v[144:145], v[72:73], v[56:57], v[116:117] op_sel_hi:[0,1,1]
	v_pk_fma_f32 v[120:121], v[32:33], v[66:67], v[120:121] op_sel:[1,0,0]
	v_pk_fma_f32 v[144:145], v[72:73], v[66:67], v[144:145] op_sel:[1,0,0]
	v_pk_fma_f32 v[120:121], v[34:35], v[70:71], v[120:121] op_sel_hi:[0,1,1]
	v_pk_fma_f32 v[144:145], v[74:75], v[70:71], v[144:145] op_sel_hi:[0,1,1]
	v_pk_fma_f32 v[116:117], v[156:157], v[56:57], v[116:117] op_sel_hi:[0,1,1]
	v_pk_fma_f32 v[116:117], v[156:157], v[66:67], v[116:117] op_sel:[1,0,0]
	v_pk_fma_f32 v[116:117], v[158:159], v[70:71], v[116:117] op_sel_hi:[0,1,1]
	v_cndmask_b32_e64 v78, 0, v18, s[10:11]
	v_cndmask_b32_e64 v79, 0, v18, s[14:15]
	v_add_f32_dpp v116, v120, v116 wave_shl:1 row_mask:0xf bank_mask:0xf bound_ctrl:1
	v_add_f32_dpp v117, v121, v117 wave_shl:1 row_mask:0xf bank_mask:0xf bound_ctrl:1
	s_add_i32 s4, s34, 3
	s_cmpk_lt_i32 s4, 0x201
	s_cselect_b64 s[12:13], s[0:1], 0
	v_add_f32_dpp v116, v144, v116 wave_shr:1 row_mask:0xf bank_mask:0xf bound_ctrl:1
	v_add_f32_dpp v117, v145, v117 wave_shr:1 row_mask:0xf bank_mask:0xf bound_ctrl:1
	v_pk_fma_f32 v[116:117], v[54:55], v[134:135], v[116:117] op_sel_hi:[1,0,1] neg_lo:[0,0,1] neg_hi:[0,0,1]
	v_pk_add_f32 v[116:117], v[116:117], v[78:79] neg_lo:[0,1] neg_hi:[0,1]
	v_pk_mul_f32 v[86:87], v[116:117], v[116:117]
	v_add_f32_e32 v86, v86, v87
	v_cndmask_b32_e64 v87, 0, v86, s[12:13]
	v_add_f32_e32 v1, v1, v87
	s_waitcnt vmcnt(8)
	v_mov_b32_dpp v32, v148 wave_shr:1 row_mask:0xf bank_mask:0xf bound_ctrl:1
	v_mov_b32_dpp v33, v149 wave_shr:1 row_mask:0xf bank_mask:0xf bound_ctrl:1
	v_mov_b32_dpp v34, v150 wave_shr:1 row_mask:0xf bank_mask:0xf bound_ctrl:1
	v_mov_b32_dpp v72, v148 wave_shl:1 row_mask:0xf bank_mask:0xf bound_ctrl:1
	v_mov_b32_dpp v73, v149 wave_shl:1 row_mask:0xf bank_mask:0xf bound_ctrl:1
	v_mov_b32_dpp v74, v150 wave_shl:1 row_mask:0xf bank_mask:0xf bound_ctrl:1
	s_add_i32 s4, s34, 7
	s_cmpk_lt_u32 s4, 0x201
	s_cselect_b64 s[12:13], s[40:41], 0
	v_cmp_eq_u32_e64 s[14:15], s37, v17
	s_and_b64 s[14:15], s[14:15], s[12:13]
	v_cndmask_b32_e64 v29, 0, 1, s[14:15]
	v_pk_add_f32 v[54:55], v[148:149], v[32:33]
	v_pk_mul_f32 v[56:57], v[148:149], v[148:149] op_sel_hi:[0,1]
	v_or_b32_dpp v86, v29, v29 wave_shr:1 row_mask:0xf bank_mask:0xf bound_ctrl:1
	v_pk_mul_f32 v[66:67], v[148:149], v[150:151] op_sel_hi:[1,0]
	v_or_b32_dpp v86, v29, v86 wave_shl:1 row_mask:0xf bank_mask:0xf bound_ctrl:1
	v_mul_f32_e64 v70, v149, v149
	v_mul_f32_e64 v71, v150, v150
	v_or_b32_dpp v87, v86, v86 wave_shr:1 row_mask:0xf bank_mask:0xf bound_ctrl:1
	v_add_f32_e64 v78, v150, v34
	v_pk_add_f32 v[54:55], v[54:55], v[72:73]
	v_or_b32_dpp v87, v86, v87 wave_shl:1 row_mask:0xf bank_mask:0xf bound_ctrl:1
	v_or3_b32 v29, v87, v88, v89
	v_or3_b32 v29, v29, v84, v85
	s_add_i32 s4, s34, 4
	s_cmpk_lt_u32 s4, 0x1ff
	s_cselect_b64 s[12:13], s[42:43], 0
	v_cmp_ne_u32_e64 s[30:31], 0, v29
	s_and_b64 s[30:31], s[30:31], s[12:13]
	v_cndmask_b32_e64 v29, 0, 1.0, s[30:31]
	v_pk_fma_f32 v[56:57], v[32:33], v[32:33], v[56:57] op_sel_hi:[0,1,1]
	v_pk_fma_f32 v[66:67], v[32:33], v[34:35], v[66:67] op_sel_hi:[1,0,1]
	v_fma_f32 v70, v33, v33, v70
	v_fma_f32 v71, v34, v34, v71
	v_add_f32_dpp v79, v29, v29 wave_shr:1 row_mask:0xf bank_mask:0xf bound_ctrl:1
	v_add_f32_e64 v78, v78, v74
	v_pk_fma_f32 v[56:57], v[72:73], v[72:73], v[56:57] op_sel_hi:[0,1,1]
	v_pk_fma_f32 v[66:67], v[72:73], v[74:75], v[66:67] op_sel_hi:[1,0,1]
	v_fma_f32 v70, v73, v73, v70
	v_fma_f32 v71, v74, v74, v71
	v_add_f32_dpp v79, v29, v79 wave_shl:1 row_mask:0xf bank_mask:0xf bound_ctrl:1
	v_pk_add_f32 v[116:117], v[4:5], v[54:55]
	v_pk_add_f32 v[114:115], v[30:31], v[116:117]
	v_pk_add_f32 v[4:5], v[44:45], v[56:57]
	v_pk_add_f32 v[30:31], v[38:39], v[4:5]
	v_pk_add_f32 v[38:39], v[50:51], v[66:67]
	v_pk_add_f32 v[44:45], v[52:53], v[38:39]
	v_pk_add_f32 v[52:53], v[92:93], v[70:71]
	v_pk_add_f32 v[50:51], v[62:63], v[52:53]
	v_pk_add_f32 v[62:63], v[100:101], v[78:79]
	v_pk_add_f32 v[92:93], v[64:65], v[62:63]
	v_mul_f32_e64 v124, v114, v22
	v_mul_f32_e64 v125, v115, v22
	v_mul_f32_e64 v126, v92, v22
	v_fma_f32 v29, v30, v22, v26
	v_mul_f32_e64 v86, v31, v22
	v_mul_f32_e64 v64, v44, v22
	v_fma_f32 v65, v50, v22, v26
	v_mul_f32_e64 v100, v45, v22
	v_fma_f32 v101, v51, v22, v26
	v_fma_f32 v29, -v124, v124, v29
	v_fma_f32 v86, -v124, v125, v86
	v_fma_f32 v64, -v124, v126, v64
	v_fma_f32 v65, -v125, v125, v65
	v_fma_f32 v100, -v125, v126, v100
	v_fma_f32 v101, -v126, v126, v101
	v_mul_f32_e64 v118, v100, v100
	v_mul_f32_e64 v119, v86, v101
	v_mul_f32_e64 v120, v64, v65
	v_mul_f32_e64 v121, v64, v64
	v_mul_f32_e64 v144, v29, v100
	v_mul_f32_e64 v145, v86, v86
	v_fma_f32 v118, v65, v101, -v118
	v_fma_f32 v119, v64, v100, -v119
	v_fma_f32 v120, v86, v100, -v120
	v_fma_f32 v121, v29, v101, -v121
	v_fma_f32 v144, v86, v64, -v144
	v_fma_f32 v145, v29, v65, -v145
	v_mul_f32_e64 v146, v29, v118
	v_fma_f32 v146, v86, v119, v146
	v_fma_f32 v146, v64, v120, v146
	v_rcp_f32_e32 v146, v146
	v_cmp_ne_u32_e64 vcc, s37, v2
	v_mul_f32_e64 v146, v146, v22
	v_cndmask_b32_e64 v146, 0, v146, s[30:31]
	v_cndmask_b32_e64 v29, 0, v18, vcc
	v_cndmask_b32_e64 v133, 0, v22, s[30:31]
	v_mul_f32_e64 v127, v118, v146
	v_mul_f32_e64 v128, v119, v146
	v_mul_f32_e64 v129, v120, v146
	v_mul_f32_e64 v130, v121, v146
	v_mul_f32_e64 v131, v144, v146
	v_mul_f32_e64 v132, v145, v146
	v_add_f32_e64 v134, v93, v29
	v_mov_b32_e32 v135, v2
	ds_write_b128 v23, v[124:127]
	ds_write_b128 v23, v[128:131] offset:1024
	ds_write_b128 v23, v[132:135] offset:2048
	v_mov_b32_dpp v30, v96 wave_shr:1 row_mask:0xf bank_mask:0xf bound_ctrl:1
	v_mov_b32_dpp v31, v97 wave_shr:1 row_mask:0xf bank_mask:0xf bound_ctrl:1
	v_mov_b32_dpp v50, v96 wave_shl:1 row_mask:0xf bank_mask:0xf bound_ctrl:1
	v_mov_b32_dpp v51, v97 wave_shl:1 row_mask:0xf bank_mask:0xf bound_ctrl:1
	v_pk_mul_f32 v[44:45], v[96:97], v[148:149] op_sel_hi:[1,0]
	v_pk_mul_f32 v[64:65], v[96:97], v[148:149] op_sel:[0,1]
	v_pk_mul_f32 v[92:93], v[96:97], v[150:151] op_sel_hi:[1,0]
	v_pk_add_f32 v[100:101], v[96:97], v[30:31]
	v_pk_fma_f32 v[44:45], v[30:31], v[32:33], v[44:45] op_sel_hi:[1,0,1]
	v_pk_fma_f32 v[64:65], v[30:31], v[32:33], v[64:65] op_sel:[0,1,0]
	v_pk_fma_f32 v[92:93], v[30:31], v[34:35], v[92:93] op_sel_hi:[1,0,1]
	v_pk_add_f32 v[100:101], v[100:101], v[50:51]
	v_pk_fma_f32 v[44:45], v[50:51], v[72:73], v[44:45] op_sel_hi:[1,0,1]
	v_pk_fma_f32 v[64:65], v[50:51], v[72:73], v[64:65] op_sel:[0,1,0]
	v_pk_fma_f32 v[92:93], v[50:51], v[74:75], v[92:93] op_sel_hi:[1,0,1]
	s_waitcnt lgkmcnt(0)
	s_barrier
	s_add_i32 s5, s34, 9
	s_min_i32 s5, s5, 0x200
	s_mul_i32 s6, s5, 0x804
	s_add_i32 s6, s6, s35
	s_add_i32 s7, s6, 0x505014
	s_add_i32 s8, s6, 0x606018
	s_mul_i32 s9, s5, 0x180c
	s_add_i32 s9, s9, s33
	s_add_i32 s4, s34, 10
	s_min_i32 s4, s4, 0x200
	s_mul_i32 s4, s4, 0x804
	s_add_i32 s4, s4, s38
	buffer_load_dword v2, v28, s[20:23], s4 offen nt
	buffer_load_dwordx3 v[144:146], v27, s[24:27], s9 offen nt
	buffer_load_dword v30, v28, s[16:19], s7 offen nt
	buffer_load_dword v31, v28, s[16:19], s8 offen nt
	v_pk_add_f32 v[50:51], v[122:123], v[100:101]
	v_pk_add_f32 v[114:115], v[172:173], v[50:51]
	v_pk_add_f32 v[118:119], v[6:7], v[44:45]
	v_pk_add_f32 v[120:121], v[20:21], v[118:119]
	v_pk_add_f32 v[6:7], v[102:103], v[64:65]
	v_pk_add_f32 v[20:21], v[68:69], v[6:7]
	v_pk_add_f32 v[102:103], v[106:107], v[92:93]
	v_pk_add_f32 v[68:69], v[108:109], v[102:103]
	v_pk_fma_f32 v[120:121], v[124:125], v[114:115], v[120:121] op_sel_hi:[0,1,1] neg_lo:[1,0,0] neg_hi:[1,0,0]
	v_pk_fma_f32 v[20:21], v[124:125], v[114:115], v[20:21] op_sel:[1,0,0] neg_lo:[1,0,0] neg_hi:[1,0,0]
	v_pk_fma_f32 v[68:69], v[126:127], v[114:115], v[68:69] op_sel_hi:[0,1,1] neg_lo:[1,0,0] neg_hi:[1,0,0]
	v_pk_mul_f32 v[106:107], v[126:127], v[120:121] op_sel:[1,0]
	v_pk_mul_f32 v[122:123], v[128:129], v[120:121] op_sel_hi:[0,1]
	v_pk_mul_f32 v[154:155], v[128:129], v[120:121] op_sel:[1,0]
	v_pk_fma_f32 v[106:107], v[128:129], v[20:21], v[106:107] op_sel_hi:[0,1,1]
	v_pk_fma_f32 v[122:123], v[130:131], v[20:21], v[122:123] op_sel_hi:[0,1,1]
	v_pk_fma_f32 v[154:155], v[130:131], v[20:21], v[154:155] op_sel:[1,0,0]
	v_pk_fma_f32 v[106:107], v[128:129], v[68:69], v[106:107] op_sel:[1,0,0]
	v_pk_fma_f32 v[122:123], v[130:131], v[68:69], v[122:123] op_sel:[1,0,0]
	v_pk_fma_f32 v[154:155], v[132:133], v[68:69], v[154:155] op_sel_hi:[0,1,1]
	v_pk_mul_f32 v[108:109], v[124:125], v[106:107] op_sel_hi:[0,1]
	v_pk_fma_f32 v[108:109], v[124:125], v[122:123], v[108:109] op_sel:[1,0,0]
	v_pk_fma_f32 v[108:109], v[126:127], v[154:155], v[108:109] op_sel_hi:[0,1,1]
	v_pk_fma_f32 v[108:109], v[132:133], v[114:115], v[108:109] op_sel:[1,0,0] neg_lo:[0,0,1] neg_hi:[0,0,1]
	v_cmp_eq_u32_e64 s[10:11], 6, v135
	v_cmp_eq_u32_e64 s[14:15], 7, v135
	v_pk_add_f32 v[20:21], v[76:77], v[106:107]
	v_pk_add_f32 v[68:69], v[94:95], v[20:21]
	v_pk_add_f32 v[76:77], v[104:105], v[122:123]
	v_pk_add_f32 v[94:95], v[98:99], v[76:77]
	v_pk_add_f32 v[104:105], v[112:113], v[154:155]
	v_pk_add_f32 v[98:99], v[110:111], v[104:105]
	v_pk_add_f32 v[110:111], v[90:91], v[108:109]
	v_pk_add_f32 v[112:113], v[60:61], v[110:111]
	v_pk_fma_f32 v[60:61], v[8:9], v[68:69], v[112:113] op_sel_hi:[0,1,1]
	v_pk_fma_f32 v[120:121], v[40:41], v[68:69], v[112:113] op_sel_hi:[0,1,1]
	v_pk_fma_f32 v[60:61], v[8:9], v[94:95], v[60:61] op_sel:[1,0,0]
	v_pk_fma_f32 v[120:121], v[40:41], v[94:95], v[120:121] op_sel:[1,0,0]
	v_pk_fma_f32 v[60:61], v[10:11], v[98:99], v[60:61] op_sel_hi:[0,1,1]
	v_pk_fma_f32 v[120:121], v[42:43], v[98:99], v[120:121] op_sel_hi:[0,1,1]
	v_pk_fma_f32 v[112:113], v[136:137], v[68:69], v[112:113] op_sel_hi:[0,1,1]
	v_pk_fma_f32 v[112:113], v[136:137], v[94:95], v[112:113] op_sel:[1,0,0]
	v_pk_fma_f32 v[112:113], v[138:139], v[98:99], v[112:113] op_sel_hi:[0,1,1]
	v_cndmask_b32_e64 v90, 0, v18, s[10:11]
	v_cndmask_b32_e64 v91, 0, v18, s[14:15]
	v_add_f32_dpp v112, v60, v112 wave_shl:1 row_mask:0xf bank_mask:0xf bound_ctrl:1
	v_add_f32_dpp v113, v61, v113 wave_shl:1 row_mask:0xf bank_mask:0xf bound_ctrl:1
	s_add_i32 s4, s34, 4
	s_cmpk_lt_i32 s4, 0x201
	s_cselect_b64 s[12:13], s[0:1], 0
	v_add_f32_dpp v112, v120, v112 wave_shr:1 row_mask:0xf bank_mask:0xf bound_ctrl:1
	v_add_f32_dpp v113, v121, v113 wave_shr:1 row_mask:0xf bank_mask:0xf bound_ctrl:1
	v_pk_fma_f32 v[112:113], v[36:37], v[134:135], v[112:113] op_sel_hi:[1,0,1] neg_lo:[0,0,1] neg_hi:[0,0,1]
	v_pk_add_f32 v[112:113], v[112:113], v[90:91] neg_lo:[0,1] neg_hi:[0,1]
	v_pk_mul_f32 v[114:115], v[112:113], v[112:113]
	v_add_f32_e32 v114, v114, v115
	v_cndmask_b32_e64 v115, 0, v114, s[12:13]
	v_add_f32_e32 v1, v1, v115
	s_waitcnt vmcnt(8)
	v_mov_b32_dpp v8, v176 wave_shr:1 row_mask:0xf bank_mask:0xf bound_ctrl:1
	v_mov_b32_dpp v9, v177 wave_shr:1 row_mask:0xf bank_mask:0xf bound_ctrl:1
	v_mov_b32_dpp v10, v178 wave_shr:1 row_mask:0xf bank_mask:0xf bound_ctrl:1
	v_mov_b32_dpp v40, v176 wave_shl:1 row_mask:0xf bank_mask:0xf bound_ctrl:1
	v_mov_b32_dpp v41, v177 wave_shl:1 row_mask:0xf bank_mask:0xf bound_ctrl:1
	v_mov_b32_dpp v42, v178 wave_shl:1 row_mask:0xf bank_mask:0xf bound_ctrl:1
	s_add_i32 s4, s34, 8
	s_cmpk_lt_u32 s4, 0x201
	s_cselect_b64 s[12:13], s[40:41], 0
	v_cmp_eq_u32_e64 s[14:15], s37, v25
	s_and_b64 s[14:15], s[14:15], s[12:13]
	v_cndmask_b32_e64 v29, 0, 1, s[14:15]
	v_pk_add_f32 v[36:37], v[176:177], v[8:9]
	v_pk_mul_f32 v[60:61], v[176:177], v[176:177] op_sel_hi:[0,1]
	v_or_b32_dpp v85, v29, v29 wave_shr:1 row_mask:0xf bank_mask:0xf bound_ctrl:1
	v_pk_mul_f32 v[68:69], v[176:177], v[178:179] op_sel_hi:[1,0]
	v_or_b32_dpp v85, v29, v85 wave_shl:1 row_mask:0xf bank_mask:0xf bound_ctrl:1
	v_mul_f32_e64 v90, v177, v177
	v_mul_f32_e64 v91, v178, v178
	v_or_b32_dpp v86, v85, v85 wave_shr:1 row_mask:0xf bank_mask:0xf bound_ctrl:1
	v_add_f32_e64 v94, v178, v10
	v_pk_add_f32 v[36:37], v[36:37], v[40:41]
	v_or_b32_dpp v86, v85, v86 wave_shl:1 row_mask:0xf bank_mask:0xf bound_ctrl:1
	v_or3_b32 v29, v86, v87, v88
	v_or3_b32 v29, v29, v89, v84
	s_add_i32 s4, s34, 5
	s_cmpk_lt_u32 s4, 0x1ff
	s_cselect_b64 s[12:13], s[42:43], 0
	v_cmp_ne_u32_e64 s[30:31], 0, v29
	s_and_b64 s[30:31], s[30:31], s[12:13]
	v_cndmask_b32_e64 v29, 0, 1.0, s[30:31]
	v_pk_fma_f32 v[60:61], v[8:9], v[8:9], v[60:61] op_sel_hi:[0,1,1]
	v_pk_fma_f32 v[68:69], v[8:9], v[10:11], v[68:69] op_sel_hi:[1,0,1]
	v_fma_f32 v90, v9, v9, v90
	v_fma_f32 v91, v10, v10, v91
	v_add_f32_dpp v95, v29, v29 wave_shr:1 row_mask:0xf bank_mask:0xf bound_ctrl:1
	v_add_f32_e64 v94, v94, v42
	v_pk_fma_f32 v[60:61], v[40:41], v[40:41], v[60:61] op_sel_hi:[0,1,1]
	v_pk_fma_f32 v[68:69], v[40:41], v[42:43], v[68:69] op_sel_hi:[1,0,1]
	v_fma_f32 v90, v41, v41, v90
	v_fma_f32 v91, v42, v42, v91
	v_add_f32_dpp v95, v29, v95 wave_shl:1 row_mask:0xf bank_mask:0xf bound_ctrl:1
	v_pk_add_f32 v[98:99], v[116:117], v[36:37]
	v_pk_add_f32 v[112:113], v[4:5], v[60:61]
	v_pk_add_f32 v[4:5], v[38:39], v[68:69]
	v_pk_add_f32 v[38:39], v[52:53], v[90:91]
	v_pk_add_f32 v[52:53], v[62:63], v[94:95]
	v_mul_f32_e64 v124, v98, v22
	v_mul_f32_e64 v125, v99, v22
	v_mul_f32_e64 v126, v52, v22
	v_fma_f32 v29, v112, v22, v26
	v_mul_f32_e64 v85, v113, v22
	v_mul_f32_e64 v62, v4, v22
	v_fma_f32 v63, v38, v22, v26
	v_mul_f32_e64 v114, v5, v22
	v_fma_f32 v115, v39, v22, v26
	v_fma_f32 v29, -v124, v124, v29
	v_fma_f32 v85, -v124, v125, v85
	v_fma_f32 v62, -v124, v126, v62
	v_fma_f32 v63, -v125, v125, v63
	v_fma_f32 v114, -v125, v126, v114
	v_fma_f32 v115, -v126, v126, v115
	v_mul_f32_e64 v116, v114, v114
	v_mul_f32_e64 v117, v85, v115
	v_mul_f32_e64 v120, v62, v63
	v_mul_f32_e64 v121, v62, v62
	v_mul_f32_e64 v136, v29, v114
	v_mul_f32_e64 v137, v85, v85
	v_fma_f32 v116, v63, v115, -v116
	v_fma_f32 v117, v62, v114, -v117
	v_fma_f32 v120, v85, v114, -v120
	v_fma_f32 v121, v29, v115, -v121
	v_fma_f32 v136, v85, v62, -v136
	v_fma_f32 v137, v29, v63, -v137
	v_mul_f32_e64 v138, v29, v116
	v_fma_f32 v138, v85, v117, v138
	v_fma_f32 v138, v62, v120, v138
	v_rcp_f32_e32 v138, v138
	v_cmp_ne_u32_e64 vcc, s37, v3
	v_mul_f32_e64 v138, v138, v22
	v_cndmask_b32_e64 v138, 0, v138, s[30:31]
	v_cndmask_b32_e64 v29, 0, v18, vcc
	v_cndmask_b32_e64 v133, 0, v22, s[30:31]
	v_mul_f32_e64 v127, v116, v138
	v_mul_f32_e64 v128, v117, v138
	v_mul_f32_e64 v129, v120, v138
	v_mul_f32_e64 v130, v121, v138
	v_mul_f32_e64 v131, v136, v138
	v_mul_f32_e64 v132, v137, v138
	v_add_f32_e64 v134, v53, v29
	v_mov_b32_e32 v135, v3
	ds_write_b128 v23, v[124:127] offset:3072
	ds_write_b128 v23, v[128:131] offset:4096
	ds_write_b128 v23, v[132:135] offset:5120
	v_mov_b32_dpp v4, v58 wave_shr:1 row_mask:0xf bank_mask:0xf bound_ctrl:1
	v_mov_b32_dpp v5, v59 wave_shr:1 row_mask:0xf bank_mask:0xf bound_ctrl:1
	v_mov_b32_dpp v52, v58 wave_shl:1 row_mask:0xf bank_mask:0xf bound_ctrl:1
	v_mov_b32_dpp v53, v59 wave_shl:1 row_mask:0xf bank_mask:0xf bound_ctrl:1
	v_pk_mul_f32 v[38:39], v[58:59], v[176:177] op_sel_hi:[1,0]
	v_pk_mul_f32 v[62:63], v[58:59], v[176:177] op_sel:[0,1]
	v_pk_mul_f32 v[98:99], v[58:59], v[178:179] op_sel_hi:[1,0]
	v_pk_add_f32 v[114:115], v[58:59], v[4:5]
	v_pk_fma_f32 v[38:39], v[4:5], v[8:9], v[38:39] op_sel_hi:[1,0,1]
	v_pk_fma_f32 v[62:63], v[4:5], v[8:9], v[62:63] op_sel:[0,1,0]
	v_pk_fma_f32 v[98:99], v[4:5], v[10:11], v[98:99] op_sel_hi:[1,0,1]
	v_pk_add_f32 v[114:115], v[114:115], v[52:53]
	v_pk_fma_f32 v[38:39], v[52:53], v[40:41], v[38:39] op_sel_hi:[1,0,1]
	v_pk_fma_f32 v[62:63], v[52:53], v[40:41], v[62:63] op_sel:[0,1,0]
	v_pk_fma_f32 v[98:99], v[52:53], v[42:43], v[98:99] op_sel_hi:[1,0,1]
	s_waitcnt lgkmcnt(0)
	s_barrier
	s_add_i32 s5, s34, 10
	s_min_i32 s5, s5, 0x200
	s_mul_i32 s6, s5, 0x804
	s_add_i32 s6, s6, s35
	s_add_i32 s7, s6, 0x505014
	s_add_i32 s8, s6, 0x606018
	s_mul_i32 s9, s5, 0x180c
	s_add_i32 s9, s9, s33
	s_add_i32 s4, s34, 11
	s_min_i32 s4, s4, 0x200
	s_mul_i32 s4, s4, 0x804
	s_add_i32 s4, s4, s38
	buffer_load_dword v3, v28, s[20:23], s4 offen nt
	buffer_load_dwordx3 v[136:138], v27, s[24:27], s9 offen nt
	buffer_load_dword v4, v28, s[16:19], s7 offen nt
	buffer_load_dword v5, v28, s[16:19], s8 offen nt
	v_pk_add_f32 v[52:53], v[50:51], v[114:115]
	v_pk_add_f32 v[50:51], v[118:119], v[38:39]
	v_pk_add_f32 v[118:119], v[6:7], v[62:63]
	v_pk_add_f32 v[6:7], v[102:103], v[98:99]
	v_pk_fma_f32 v[50:51], v[124:125], v[52:53], v[50:51] op_sel_hi:[0,1,1] neg_lo:[1,0,0] neg_hi:[1,0,0]
	v_pk_fma_f32 v[118:119], v[124:125], v[52:53], v[118:119] op_sel:[1,0,0] neg_lo:[1,0,0] neg_hi:[1,0,0]
	v_pk_fma_f32 v[6:7], v[126:127], v[52:53], v[6:7] op_sel_hi:[0,1,1] neg_lo:[1,0,0] neg_hi:[1,0,0]
	v_pk_mul_f32 v[84:85], v[126:127], v[50:51] op_sel:[1,0]
	v_pk_mul_f32 v[112:113], v[128:129], v[50:51] op_sel_hi:[0,1]
	v_pk_mul_f32 v[116:117], v[128:129], v[50:51] op_sel:[1,0]
	v_pk_fma_f32 v[84:85], v[128:129], v[118:119], v[84:85] op_sel_hi:[0,1,1]
	v_pk_fma_f32 v[112:113], v[130:131], v[118:119], v[112:113] op_sel_hi:[0,1,1]
	v_pk_fma_f32 v[116:117], v[130:131], v[118:119], v[116:117] op_sel:[1,0,0]
	v_pk_fma_f32 v[84:85], v[128:129], v[6:7], v[84:85] op_sel:[1,0,0]
	v_pk_fma_f32 v[112:113], v[130:131], v[6:7], v[112:113] op_sel:[1,0,0]
	v_pk_fma_f32 v[116:117], v[132:133], v[6:7], v[116:117] op_sel_hi:[0,1,1]
	v_pk_mul_f32 v[102:103], v[124:125], v[84:85] op_sel_hi:[0,1]
	v_pk_fma_f32 v[102:103], v[124:125], v[112:113], v[102:103] op_sel:[1,0,0]
	v_pk_fma_f32 v[102:103], v[126:127], v[116:117], v[102:103] op_sel_hi:[0,1,1]
	v_pk_fma_f32 v[102:103], v[132:133], v[52:53], v[102:103] op_sel:[1,0,0] neg_lo:[0,0,1] neg_hi:[0,0,1]
	v_cmp_eq_u32_e64 s[10:11], 6, v135
	v_cmp_eq_u32_e64 s[14:15], 7, v135
	v_pk_add_f32 v[6:7], v[20:21], v[84:85]
	v_pk_add_f32 v[20:21], v[76:77], v[112:113]
	v_pk_add_f32 v[50:51], v[104:105], v[116:117]
	v_pk_add_f32 v[52:53], v[110:111], v[102:103]
	v_pk_fma_f32 v[76:77], v[12:13], v[6:7], v[52:53] op_sel_hi:[0,1,1]
	v_pk_fma_f32 v[104:105], v[80:81], v[6:7], v[52:53] op_sel_hi:[0,1,1]
	v_pk_fma_f32 v[76:77], v[12:13], v[20:21], v[76:77] op_sel:[1,0,0]
	v_pk_fma_f32 v[104:105], v[80:81], v[20:21], v[104:105] op_sel:[1,0,0]
	v_pk_fma_f32 v[76:77], v[14:15], v[50:51], v[76:77] op_sel_hi:[0,1,1]
	v_pk_fma_f32 v[104:105], v[82:83], v[50:51], v[104:105] op_sel_hi:[0,1,1]
	v_pk_fma_f32 v[52:53], v[168:169], v[6:7], v[52:53] op_sel_hi:[0,1,1]
	v_pk_fma_f32 v[52:53], v[168:169], v[20:21], v[52:53] op_sel:[1,0,0]
	v_pk_fma_f32 v[52:53], v[170:171], v[50:51], v[52:53] op_sel_hi:[0,1,1]
	v_cndmask_b32_e64 v110, 0, v18, s[10:11]
	v_cndmask_b32_e64 v111, 0, v18, s[14:15]
	v_add_f32_dpp v52, v76, v52 wave_shl:1 row_mask:0xf bank_mask:0xf bound_ctrl:1
	v_add_f32_dpp v53, v77, v53 wave_shl:1 row_mask:0xf bank_mask:0xf bound_ctrl:1
	s_add_i32 s4, s34, 5
	s_cmpk_lt_i32 s4, 0x201
	s_cselect_b64 s[12:13], s[0:1], 0
	v_add_f32_dpp v52, v104, v52 wave_shr:1 row_mask:0xf bank_mask:0xf bound_ctrl:1
	v_add_f32_dpp v53, v105, v53 wave_shr:1 row_mask:0xf bank_mask:0xf bound_ctrl:1
	v_pk_fma_f32 v[52:53], v[46:47], v[134:135], v[52:53] op_sel_hi:[1,0,1] neg_lo:[0,0,1] neg_hi:[0,0,1]
	v_pk_add_f32 v[52:53], v[52:53], v[110:111] neg_lo:[0,1] neg_hi:[0,1]
	v_pk_mul_f32 v[118:119], v[52:53], v[52:53]
	v_add_f32_e32 v118, v118, v119
	v_cndmask_b32_e64 v119, 0, v118, s[12:13]
	v_add_f32_e32 v1, v1, v119
	s_waitcnt vmcnt(8)
	v_mov_b32_dpp v12, v140 wave_shr:1 row_mask:0xf bank_mask:0xf bound_ctrl:1
	v_mov_b32_dpp v13, v141 wave_shr:1 row_mask:0xf bank_mask:0xf bound_ctrl:1
	v_mov_b32_dpp v14, v142 wave_shr:1 row_mask:0xf bank_mask:0xf bound_ctrl:1
	v_mov_b32_dpp v80, v140 wave_shl:1 row_mask:0xf bank_mask:0xf bound_ctrl:1
	v_mov_b32_dpp v81, v141 wave_shl:1 row_mask:0xf bank_mask:0xf bound_ctrl:1
	v_mov_b32_dpp v82, v142 wave_shl:1 row_mask:0xf bank_mask:0xf bound_ctrl:1
	s_add_i32 s4, s34, 9
	s_cmpk_lt_u32 s4, 0x201
	s_cselect_b64 s[12:13], s[40:41], 0
	v_cmp_eq_u32_e64 s[14:15], s37, v24
	s_and_b64 s[14:15], s[14:15], s[12:13]
	v_cndmask_b32_e64 v29, 0, 1, s[14:15]
	v_pk_add_f32 v[6:7], v[140:141], v[12:13]
	v_pk_mul_f32 v[20:21], v[140:141], v[140:141] op_sel_hi:[0,1]
	v_or_b32_dpp v76, v29, v29 wave_shr:1 row_mask:0xf bank_mask:0xf bound_ctrl:1
	v_pk_mul_f32 v[46:47], v[140:141], v[142:143] op_sel_hi:[1,0]
	v_or_b32_dpp v76, v29, v76 wave_shl:1 row_mask:0xf bank_mask:0xf bound_ctrl:1
	v_mul_f32_e64 v50, v141, v141
	v_mul_f32_e64 v51, v142, v142
	v_or_b32_dpp v77, v76, v76 wave_shr:1 row_mask:0xf bank_mask:0xf bound_ctrl:1
	v_add_f32_e64 v52, v142, v14
	v_pk_add_f32 v[6:7], v[6:7], v[80:81]
	v_or_b32_dpp v77, v76, v77 wave_shl:1 row_mask:0xf bank_mask:0xf bound_ctrl:1
	v_or3_b32 v29, v77, v86, v87
	v_or3_b32 v29, v29, v88, v89
	s_add_i32 s4, s34, 6
	s_cmpk_lt_u32 s4, 0x1ff
	s_cselect_b64 s[12:13], s[42:43], 0
	v_cmp_ne_u32_e64 s[30:31], 0, v29
	s_and_b64 s[30:31], s[30:31], s[12:13]
	v_cndmask_b32_e64 v29, 0, 1.0, s[30:31]
	v_pk_fma_f32 v[20:21], v[12:13], v[12:13], v[20:21] op_sel_hi:[0,1,1]
	v_pk_fma_f32 v[46:47], v[12:13], v[14:15], v[46:47] op_sel_hi:[1,0,1]
	v_fma_f32 v50, v13, v13, v50
	v_fma_f32 v51, v14, v14, v51
	v_add_f32_dpp v53, v29, v29 wave_shr:1 row_mask:0xf bank_mask:0xf bound_ctrl:1
	v_add_f32_e64 v52, v52, v82
	v_pk_fma_f32 v[20:21], v[80:81], v[80:81], v[20:21] op_sel_hi:[0,1,1]
	v_pk_fma_f32 v[46:47], v[80:81], v[82:83], v[46:47] op_sel_hi:[1,0,1]
	v_fma_f32 v50, v81, v81, v50
	v_fma_f32 v51, v82, v82, v51
	v_add_f32_dpp v53, v29, v53 wave_shl:1 row_mask:0xf bank_mask:0xf bound_ctrl:1
	v_pk_add_f32 v[104:105], v[36:37], v[6:7]
	v_pk_add_f32 v[110:111], v[54:55], v[104:105]
	v_pk_add_f32 v[54:55], v[60:61], v[20:21]
	v_pk_add_f32 v[36:37], v[56:57], v[54:55]
	v_pk_add_f32 v[56:57], v[68:69], v[46:47]
	v_pk_add_f32 v[60:61], v[66:67], v[56:57]
	v_pk_add_f32 v[68:69], v[90:91], v[50:51]
	v_pk_add_f32 v[66:67], v[70:71], v[68:69]
	v_pk_add_f32 v[120:121], v[94:95], v[52:53]
	v_pk_add_f32 v[70:71], v[78:79], v[120:121]
	v_mul_f32_e64 v124, v110, v22
	v_mul_f32_e64 v125, v111, v22
	v_mul_f32_e64 v126, v70, v22
	v_fma_f32 v29, v36, v22, v26
	v_mul_f32_e64 v76, v37, v22
	v_mul_f32_e64 v78, v60, v22
	v_fma_f32 v79, v66, v22, v26
	v_mul_f32_e64 v90, v61, v22
	v_fma_f32 v91, v67, v22, v26
	v_fma_f32 v29, -v124, v124, v29
	v_fma_f32 v76, -v124, v125, v76
	v_fma_f32 v78, -v124, v126, v78
	v_fma_f32 v79, -v125, v125, v79
	v_fma_f32 v90, -v125, v126, v90
	v_fma_f32 v91, -v126, v126, v91
	v_mul_f32_e64 v94, v90, v90
	v_mul_f32_e64 v95, v76, v91
	v_mul_f32_e64 v118, v78, v79
	v_mul_f32_e64 v119, v78, v78
	v_mul_f32_e64 v152, v29, v90
	v_mul_f32_e64 v153, v76, v76
	v_fma_f32 v94, v79, v91, -v94
	v_fma_f32 v95, v78, v90, -v95
	v_fma_f32 v118, v76, v90, -v118
	v_fma_f32 v119, v29, v91, -v119
	v_fma_f32 v152, v76, v78, -v152
	v_fma_f32 v153, v29, v79, -v153
	v_mul_f32_e64 v156, v29, v94
	v_fma_f32 v156, v76, v95, v156
	v_fma_f32 v156, v78, v118, v156
	v_rcp_f32_e32 v156, v156
	v_cmp_ne_u32_e64 vcc, s37, v16
	v_mul_f32_e64 v156, v156, v22
	v_cndmask_b32_e64 v156, 0, v156, s[30:31]
	v_cndmask_b32_e64 v29, 0, v18, vcc
	v_cndmask_b32_e64 v133, 0, v22, s[30:31]
	v_mul_f32_e64 v127, v94, v156
	v_mul_f32_e64 v128, v95, v156
	v_mul_f32_e64 v129, v118, v156
	v_mul_f32_e64 v130, v119, v156
	v_mul_f32_e64 v131, v152, v156
	v_mul_f32_e64 v132, v153, v156
	v_add_f32_e64 v134, v71, v29
	v_mov_b32_e32 v135, v16
	ds_write_b128 v23, v[124:127]
	ds_write_b128 v23, v[128:131] offset:1024
	ds_write_b128 v23, v[132:135] offset:2048
	v_mov_b32_dpp v66, v48 wave_shr:1 row_mask:0xf bank_mask:0xf bound_ctrl:1
	v_mov_b32_dpp v67, v49 wave_shr:1 row_mask:0xf bank_mask:0xf bound_ctrl:1
	v_mov_b32_dpp v70, v48 wave_shl:1 row_mask:0xf bank_mask:0xf bound_ctrl:1
	v_mov_b32_dpp v71, v49 wave_shl:1 row_mask:0xf bank_mask:0xf bound_ctrl:1
	v_pk_mul_f32 v[36:37], v[48:49], v[140:141] op_sel_hi:[1,0]
	v_pk_mul_f32 v[60:61], v[48:49], v[140:141] op_sel:[0,1]
	v_pk_mul_f32 v[152:153], v[48:49], v[142:143] op_sel_hi:[1,0]
	v_pk_add_f32 v[156:157], v[48:49], v[66:67]
	v_pk_fma_f32 v[36:37], v[66:67], v[12:13], v[36:37] op_sel_hi:[1,0,1]
	v_pk_fma_f32 v[60:61], v[66:67], v[12:13], v[60:61] op_sel:[0,1,0]
	v_pk_fma_f32 v[152:153], v[66:67], v[14:15], v[152:153] op_sel_hi:[1,0,1]
	v_pk_add_f32 v[156:157], v[156:157], v[70:71]
	v_pk_fma_f32 v[36:37], v[70:71], v[80:81], v[36:37] op_sel_hi:[1,0,1]
	v_pk_fma_f32 v[60:61], v[70:71], v[80:81], v[60:61] op_sel:[0,1,0]
	v_pk_fma_f32 v[152:153], v[70:71], v[82:83], v[152:153] op_sel_hi:[1,0,1]
	s_waitcnt lgkmcnt(0)
	s_barrier
	s_add_i32 s5, s34, 11
	s_min_i32 s5, s5, 0x200
	s_mul_i32 s6, s5, 0x804
	s_add_i32 s6, s6, s35
	s_add_i32 s7, s6, 0x505014
	s_add_i32 s8, s6, 0x606018
	s_mul_i32 s9, s5, 0x180c
	s_add_i32 s9, s9, s33
	s_add_i32 s4, s34, 12
	s_min_i32 s4, s4, 0x200
	s_mul_i32 s4, s4, 0x804
	s_add_i32 s4, s4, s38
	buffer_load_dword v16, v28, s[20:23], s4 offen nt
	buffer_load_dwordx3 v[160:162], v27, s[24:27], s9 offen nt
	buffer_load_dword v66, v28, s[16:19], s7 offen nt
	buffer_load_dword v67, v28, s[16:19], s8 offen nt
	v_pk_add_f32 v[70:71], v[114:115], v[156:157]
	v_pk_add_f32 v[78:79], v[100:101], v[70:71]
	v_pk_add_f32 v[90:91], v[38:39], v[36:37]
	v_pk_add_f32 v[100:101], v[44:45], v[90:91]
	v_pk_add_f32 v[38:39], v[62:63], v[60:61]
	v_pk_add_f32 v[44:45], v[64:65], v[38:39]
	v_pk_add_f32 v[62:63], v[98:99], v[152:153]
	v_pk_add_f32 v[64:65], v[92:93], v[62:63]
	v_pk_fma_f32 v[100:101], v[124:125], v[78:79], v[100:101] op_sel_hi:[0,1,1] neg_lo:[1,0,0] neg_hi:[1,0,0]
	v_pk_fma_f32 v[44:45], v[124:125], v[78:79], v[44:45] op_sel:[1,0,0] neg_lo:[1,0,0] neg_hi:[1,0,0]
	v_pk_fma_f32 v[64:65], v[126:127], v[78:79], v[64:65] op_sel_hi:[0,1,1] neg_lo:[1,0,0] neg_hi:[1,0,0]
	v_pk_mul_f32 v[94:95], v[126:127], v[100:101] op_sel:[1,0]
	v_pk_mul_f32 v[98:99], v[128:129], v[100:101] op_sel_hi:[0,1]
	v_pk_mul_f32 v[110:111], v[128:129], v[100:101] op_sel:[1,0]
	v_pk_fma_f32 v[94:95], v[128:129], v[44:45], v[94:95] op_sel_hi:[0,1,1]
	v_pk_fma_f32 v[98:99], v[130:131], v[44:45], v[98:99] op_sel_hi:[0,1,1]
	v_pk_fma_f32 v[110:111], v[130:131], v[44:45], v[110:111] op_sel:[1,0,0]
	v_pk_fma_f32 v[94:95], v[128:129], v[64:65], v[94:95] op_sel:[1,0,0]
	v_pk_fma_f32 v[98:99], v[130:131], v[64:65], v[98:99] op_sel:[1,0,0]
	v_pk_fma_f32 v[110:111], v[132:133], v[64:65], v[110:111] op_sel_hi:[0,1,1]
	v_pk_mul_f32 v[92:93], v[124:125], v[94:95] op_sel_hi:[0,1]
	v_pk_fma_f32 v[92:93], v[124:125], v[98:99], v[92:93] op_sel:[1,0,0]
	v_pk_fma_f32 v[92:93], v[126:127], v[110:111], v[92:93] op_sel_hi:[0,1,1]
	v_pk_fma_f32 v[92:93], v[132:133], v[78:79], v[92:93] op_sel:[1,0,0] neg_lo:[0,0,1] neg_hi:[0,0,1]
	v_cmp_eq_u32_e64 s[10:11], 6, v135
	v_cmp_eq_u32_e64 s[14:15], 7, v135
	v_pk_add_f32 v[44:45], v[84:85], v[94:95]
	v_pk_add_f32 v[64:65], v[106:107], v[44:45]
	v_pk_add_f32 v[84:85], v[112:113], v[98:99]
	v_pk_add_f32 v[78:79], v[122:123], v[84:85]
	v_pk_add_f32 v[100:101], v[116:117], v[110:111]
	v_pk_add_f32 v[106:107], v[154:155], v[100:101]
	v_pk_add_f32 v[114:115], v[102:103], v[92:93]
	v_pk_add_f32 v[112:113], v[108:109], v[114:115]
	v_pk_fma_f32 v[108:109], v[32:33], v[64:65], v[112:113] op_sel_hi:[0,1,1]
	v_pk_fma_f32 v[116:117], v[72:73], v[64:65], v[112:113] op_sel_hi:[0,1,1]
	v_pk_fma_f32 v[108:109], v[32:33], v[78:79], v[108:109] op_sel:[1,0,0]
	v_pk_fma_f32 v[116:117], v[72:73], v[78:79], v[116:117] op_sel:[1,0,0]
	v_pk_fma_f32 v[108:109], v[34:35], v[106:107], v[108:109] op_sel_hi:[0,1,1]
	v_pk_fma_f32 v[116:117], v[74:75], v[106:107], v[116:117] op_sel_hi:[0,1,1]
	v_pk_fma_f32 v[112:113], v[148:149], v[64:65], v[112:113] op_sel_hi:[0,1,1]
	v_pk_fma_f32 v[112:113], v[148:149], v[78:79], v[112:113] op_sel:[1,0,0]
	v_pk_fma_f32 v[112:113], v[150:151], v[106:107], v[112:113] op_sel_hi:[0,1,1]
	v_cndmask_b32_e64 v102, 0, v18, s[10:11]
	v_cndmask_b32_e64 v103, 0, v18, s[14:15]
	v_add_f32_dpp v112, v108, v112 wave_shl:1 row_mask:0xf bank_mask:0xf bound_ctrl:1
	v_add_f32_dpp v113, v109, v113 wave_shl:1 row_mask:0xf bank_mask:0xf bound_ctrl:1
	s_add_i32 s4, s34, 6
	s_cmpk_lt_i32 s4, 0x201
	s_cselect_b64 s[12:13], s[0:1], 0
	v_add_f32_dpp v112, v116, v112 wave_shr:1 row_mask:0xf bank_mask:0xf bound_ctrl:1
	v_add_f32_dpp v113, v117, v113 wave_shr:1 row_mask:0xf bank_mask:0xf bound_ctrl:1
	v_pk_fma_f32 v[112:113], v[96:97], v[134:135], v[112:113] op_sel_hi:[1,0,1] neg_lo:[0,0,1] neg_hi:[0,0,1]
	v_pk_add_f32 v[112:113], v[112:113], v[102:103] neg_lo:[0,1] neg_hi:[0,1]
	v_pk_mul_f32 v[118:119], v[112:113], v[112:113]
	v_add_f32_e32 v118, v118, v119
	v_cndmask_b32_e64 v119, 0, v118, s[12:13]
	v_add_f32_e32 v1, v1, v119
	s_waitcnt vmcnt(8)
	v_mov_b32_dpp v32, v144 wave_shr:1 row_mask:0xf bank_mask:0xf bound_ctrl:1
	v_mov_b32_dpp v33, v145 wave_shr:1 row_mask:0xf bank_mask:0xf bound_ctrl:1
	v_mov_b32_dpp v34, v146 wave_shr:1 row_mask:0xf bank_mask:0xf bound_ctrl:1
	v_mov_b32_dpp v72, v144 wave_shl:1 row_mask:0xf bank_mask:0xf bound_ctrl:1
	v_mov_b32_dpp v73, v145 wave_shl:1 row_mask:0xf bank_mask:0xf bound_ctrl:1
	v_mov_b32_dpp v74, v146 wave_shl:1 row_mask:0xf bank_mask:0xf bound_ctrl:1
	s_add_i32 s4, s34, 10
	s_cmpk_lt_u32 s4, 0x201
	s_cselect_b64 s[12:13], s[40:41], 0
	v_cmp_eq_u32_e64 s[14:15], s37, v2
	s_and_b64 s[14:15], s[14:15], s[12:13]
	v_cndmask_b32_e64 v29, 0, 1, s[14:15]
	v_pk_add_f32 v[64:65], v[144:145], v[32:33]
	v_pk_mul_f32 v[78:79], v[144:145], v[144:145] op_sel_hi:[0,1]
	v_or_b32_dpp v76, v29, v29 wave_shr:1 row_mask:0xf bank_mask:0xf bound_ctrl:1
	v_pk_mul_f32 v[96:97], v[144:145], v[146:147] op_sel_hi:[1,0]
	v_or_b32_dpp v76, v29, v76 wave_shl:1 row_mask:0xf bank_mask:0xf bound_ctrl:1
	v_mul_f32_e64 v102, v145, v145
	v_mul_f32_e64 v103, v146, v146
	v_or_b32_dpp v89, v76, v76 wave_shr:1 row_mask:0xf bank_mask:0xf bound_ctrl:1
	v_add_f32_e64 v106, v146, v34
	v_pk_add_f32 v[64:65], v[64:65], v[72:73]
	v_or_b32_dpp v89, v76, v89 wave_shl:1 row_mask:0xf bank_mask:0xf bound_ctrl:1
	v_or3_b32 v29, v89, v77, v86
	v_or3_b32 v29, v29, v87, v88
	s_add_i32 s4, s34, 7
	s_cmpk_lt_u32 s4, 0x1ff
	s_cselect_b64 s[12:13], s[42:43], 0
	v_cmp_ne_u32_e64 s[30:31], 0, v29
	s_and_b64 s[30:31], s[30:31], s[12:13]
	v_cndmask_b32_e64 v29, 0, 1.0, s[30:31]
	v_pk_fma_f32 v[78:79], v[32:33], v[32:33], v[78:79] op_sel_hi:[0,1,1]
	v_pk_fma_f32 v[96:97], v[32:33], v[34:35], v[96:97] op_sel_hi:[1,0,1]
	v_fma_f32 v102, v33, v33, v102
	v_fma_f32 v103, v34, v34, v103
	v_add_f32_dpp v107, v29, v29 wave_shr:1 row_mask:0xf bank_mask:0xf bound_ctrl:1
	v_add_f32_e64 v106, v106, v74
	v_pk_fma_f32 v[78:79], v[72:73], v[72:73], v[78:79] op_sel_hi:[0,1,1]
	v_pk_fma_f32 v[96:97], v[72:73], v[74:75], v[96:97] op_sel_hi:[1,0,1]
	v_fma_f32 v102, v73, v73, v102
	v_fma_f32 v103, v74, v74, v103
	v_add_f32_dpp v107, v29, v107 wave_shl:1 row_mask:0xf bank_mask:0xf bound_ctrl:1
	v_pk_add_f32 v[108:109], v[104:105], v[64:65]
	v_pk_add_f32 v[104:105], v[54:55], v[78:79]
	v_pk_add_f32 v[54:55], v[56:57], v[96:97]
	v_pk_add_f32 v[56:57], v[68:69], v[102:103]
	v_pk_add_f32 v[68:69], v[120:121], v[106:107]
	v_mul_f32_e64 v116, v108, v22
	v_mul_f32_e64 v117, v109, v22
	v_mul_f32_e64 v118, v68, v22
	v_fma_f32 v29, v104, v22, v26
	v_mul_f32_e64 v76, v105, v22
	v_mul_f32_e64 v112, v54, v22
	v_fma_f32 v113, v56, v22, v26
	v_mul_f32_e64 v128, v55, v22
	v_fma_f32 v129, v57, v22, v26
	v_fma_f32 v29, -v116, v116, v29
	v_fma_f32 v76, -v116, v117, v76
	v_fma_f32 v112, -v116, v118, v112
	v_fma_f32 v113, -v117, v117, v113
	v_fma_f32 v128, -v117, v118, v128
	v_fma_f32 v129, -v118, v118, v129
	v_mul_f32_e64 v130, v128, v128
	v_mul_f32_e64 v131, v76, v129
	v_mul_f32_e64 v132, v112, v113
	v_mul_f32_e64 v133, v112, v112
	v_mul_f32_e64 v134, v29, v128
	v_mul_f32_e64 v135, v76, v76
	v_fma_f32 v130, v113, v129, -v130
	v_fma_f32 v131, v112, v128, -v131
	v_fma_f32 v132, v76, v128, -v132
	v_fma_f32 v133, v29, v129, -v133
	v_fma_f32 v134, v76, v112, -v134
	v_fma_f32 v135, v29, v113, -v135
	v_mul_f32_e64 v148, v29, v130
	v_fma_f32 v148, v76, v131, v148
	v_fma_f32 v148, v112, v132, v148
	v_rcp_f32_e32 v148, v148
	v_cmp_ne_u32_e64 vcc, s37, v17
	v_mul_f32_e64 v148, v148, v22
	v_cndmask_b32_e64 v148, 0, v148, s[30:31]
	v_cndmask_b32_e64 v29, 0, v18, vcc
	v_cndmask_b32_e64 v125, 0, v22, s[30:31]
	v_mul_f32_e64 v119, v130, v148
	v_mul_f32_e64 v120, v131, v148
	v_mul_f32_e64 v121, v132, v148
	v_mul_f32_e64 v122, v133, v148
	v_mul_f32_e64 v123, v134, v148
	v_mul_f32_e64 v124, v135, v148
	v_add_f32_e64 v126, v69, v29
	v_mov_b32_e32 v127, v17
	ds_write_b128 v23, v[116:119] offset:3072
	ds_write_b128 v23, v[120:123] offset:4096
	ds_write_b128 v23, v[124:127] offset:5120
	v_mov_b32_dpp v56, v30 wave_shr:1 row_mask:0xf bank_mask:0xf bound_ctrl:1
	v_mov_b32_dpp v57, v31 wave_shr:1 row_mask:0xf bank_mask:0xf bound_ctrl:1
	v_mov_b32_dpp v68, v30 wave_shl:1 row_mask:0xf bank_mask:0xf bound_ctrl:1
	v_mov_b32_dpp v69, v31 wave_shl:1 row_mask:0xf bank_mask:0xf bound_ctrl:1
	v_pk_mul_f32 v[54:55], v[30:31], v[144:145] op_sel_hi:[1,0]
	v_pk_mul_f32 v[130:131], v[30:31], v[144:145] op_sel:[0,1]
	v_pk_mul_f32 v[134:135], v[30:31], v[146:147] op_sel_hi:[1,0]
	v_pk_add_f32 v[150:151], v[30:31], v[56:57]
	v_pk_fma_f32 v[54:55], v[56:57], v[32:33], v[54:55] op_sel_hi:[1,0,1]
	v_pk_fma_f32 v[130:131], v[56:57], v[32:33], v[130:131] op_sel:[0,1,0]
	v_pk_fma_f32 v[134:135], v[56:57], v[34:35], v[134:135] op_sel_hi:[1,0,1]
	v_pk_add_f32 v[150:151], v[150:151], v[68:69]
	v_pk_fma_f32 v[54:55], v[68:69], v[72:73], v[54:55] op_sel_hi:[1,0,1]
	v_pk_fma_f32 v[130:131], v[68:69], v[72:73], v[130:131] op_sel:[0,1,0]
	v_pk_fma_f32 v[134:135], v[68:69], v[74:75], v[134:135] op_sel_hi:[1,0,1]
	s_waitcnt lgkmcnt(0)
	s_barrier
	v_pk_add_f32 v[56:57], v[70:71], v[150:151]
	v_pk_add_f32 v[70:71], v[90:91], v[54:55]
	v_pk_add_f32 v[90:91], v[38:39], v[130:131]
	v_pk_add_f32 v[38:39], v[62:63], v[134:135]
	v_pk_fma_f32 v[70:71], v[116:117], v[56:57], v[70:71] op_sel_hi:[0,1,1] neg_lo:[1,0,0] neg_hi:[1,0,0]
	v_pk_fma_f32 v[90:91], v[116:117], v[56:57], v[90:91] op_sel:[1,0,0] neg_lo:[1,0,0] neg_hi:[1,0,0]
	v_pk_fma_f32 v[38:39], v[118:119], v[56:57], v[38:39] op_sel_hi:[0,1,1] neg_lo:[1,0,0] neg_hi:[1,0,0]
	v_pk_mul_f32 v[68:69], v[118:119], v[70:71] op_sel:[1,0]
	v_pk_mul_f32 v[104:105], v[120:121], v[70:71] op_sel_hi:[0,1]
	v_pk_mul_f32 v[108:109], v[120:121], v[70:71] op_sel:[1,0]
	v_pk_fma_f32 v[68:69], v[120:121], v[90:91], v[68:69] op_sel_hi:[0,1,1]
	v_pk_fma_f32 v[104:105], v[122:123], v[90:91], v[104:105] op_sel_hi:[0,1,1]
	v_pk_fma_f32 v[108:109], v[122:123], v[90:91], v[108:109] op_sel:[1,0,0]
	v_pk_fma_f32 v[68:69], v[120:121], v[38:39], v[68:69] op_sel:[1,0,0]
	v_pk_fma_f32 v[104:105], v[122:123], v[38:39], v[104:105] op_sel:[1,0,0]
	v_pk_fma_f32 v[108:109], v[124:125], v[38:39], v[108:109] op_sel_hi:[0,1,1]
	v_pk_mul_f32 v[62:63], v[116:117], v[68:69] op_sel_hi:[0,1]
	v_pk_fma_f32 v[62:63], v[116:117], v[104:105], v[62:63] op_sel:[1,0,0]
	v_pk_fma_f32 v[62:63], v[118:119], v[108:109], v[62:63] op_sel_hi:[0,1,1]
	v_pk_fma_f32 v[62:63], v[124:125], v[56:57], v[62:63] op_sel:[1,0,0] neg_lo:[0,0,1] neg_hi:[0,0,1]
	v_cmp_eq_u32_e64 s[10:11], 6, v127
	v_cmp_eq_u32_e64 s[14:15], 7, v127
	v_pk_add_f32 v[38:39], v[44:45], v[68:69]
	v_pk_add_f32 v[44:45], v[84:85], v[104:105]
	v_pk_add_f32 v[56:57], v[100:101], v[108:109]
	v_pk_add_f32 v[70:71], v[114:115], v[62:63]
	v_pk_fma_f32 v[90:91], v[8:9], v[38:39], v[70:71] op_sel_hi:[0,1,1]
	v_pk_fma_f32 v[114:115], v[40:41], v[38:39], v[70:71] op_sel_hi:[0,1,1]
	v_pk_fma_f32 v[90:91], v[8:9], v[44:45], v[90:91] op_sel:[1,0,0]
	v_pk_fma_f32 v[114:115], v[40:41], v[44:45], v[114:115] op_sel:[1,0,0]
	v_pk_fma_f32 v[90:91], v[10:11], v[56:57], v[90:91] op_sel_hi:[0,1,1]
	v_pk_fma_f32 v[114:115], v[42:43], v[56:57], v[114:115] op_sel_hi:[0,1,1]
	v_pk_fma_f32 v[70:71], v[176:177], v[38:39], v[70:71] op_sel_hi:[0,1,1]
	v_pk_fma_f32 v[70:71], v[176:177], v[44:45], v[70:71] op_sel:[1,0,0]
	v_pk_fma_f32 v[70:71], v[178:179], v[56:57], v[70:71] op_sel_hi:[0,1,1]
	v_cndmask_b32_e64 v84, 0, v18, s[10:11]
	v_cndmask_b32_e64 v85, 0, v18, s[14:15]
	v_add_f32_dpp v70, v90, v70 wave_shl:1 row_mask:0xf bank_mask:0xf bound_ctrl:1
	v_add_f32_dpp v71, v91, v71 wave_shl:1 row_mask:0xf bank_mask:0xf bound_ctrl:1
	s_add_i32 s4, s34, 7
	s_cmpk_lt_i32 s4, 0x201
	s_cselect_b64 s[12:13], s[0:1], 0
	v_add_f32_dpp v70, v114, v70 wave_shr:1 row_mask:0xf bank_mask:0xf bound_ctrl:1
	v_add_f32_dpp v71, v115, v71 wave_shr:1 row_mask:0xf bank_mask:0xf bound_ctrl:1
	v_pk_fma_f32 v[70:71], v[58:59], v[126:127], v[70:71] op_sel_hi:[1,0,1] neg_lo:[0,0,1] neg_hi:[0,0,1]
	v_pk_add_f32 v[70:71], v[70:71], v[84:85] neg_lo:[0,1] neg_hi:[0,1]
	v_pk_mul_f32 v[100:101], v[70:71], v[70:71]
	v_add_f32_e32 v100, v100, v101
	v_cndmask_b32_e64 v101, 0, v100, s[12:13]
	v_add_f32_e32 v1, v1, v101
	s_waitcnt vmcnt(4)
	v_mov_b32_dpp v8, v136 wave_shr:1 row_mask:0xf bank_mask:0xf bound_ctrl:1
	v_mov_b32_dpp v9, v137 wave_shr:1 row_mask:0xf bank_mask:0xf bound_ctrl:1
	v_mov_b32_dpp v10, v138 wave_shr:1 row_mask:0xf bank_mask:0xf bound_ctrl:1
	v_mov_b32_dpp v40, v136 wave_shl:1 row_mask:0xf bank_mask:0xf bound_ctrl:1
	v_mov_b32_dpp v41, v137 wave_shl:1 row_mask:0xf bank_mask:0xf bound_ctrl:1
	v_mov_b32_dpp v42, v138 wave_shl:1 row_mask:0xf bank_mask:0xf bound_ctrl:1
	s_add_i32 s4, s34, 11
	s_cmpk_lt_u32 s4, 0x201
	s_cselect_b64 s[12:13], s[40:41], 0
	v_cmp_eq_u32_e64 s[14:15], s37, v3
	s_and_b64 s[14:15], s[14:15], s[12:13]
	v_cndmask_b32_e64 v17, 0, 1, s[14:15]
	v_pk_add_f32 v[38:39], v[136:137], v[8:9]
	v_pk_mul_f32 v[44:45], v[136:137], v[136:137] op_sel_hi:[0,1]
	v_or_b32_dpp v29, v17, v17 wave_shr:1 row_mask:0xf bank_mask:0xf bound_ctrl:1
	v_pk_mul_f32 v[56:57], v[136:137], v[138:139] op_sel_hi:[1,0]
	v_or_b32_dpp v29, v17, v29 wave_shl:1 row_mask:0xf bank_mask:0xf bound_ctrl:1
	v_mul_f32_e64 v58, v137, v137
	v_mul_f32_e64 v59, v138, v138
	v_or_b32_dpp v76, v29, v29 wave_shr:1 row_mask:0xf bank_mask:0xf bound_ctrl:1
	v_add_f32_e64 v70, v138, v10
	v_pk_add_f32 v[38:39], v[38:39], v[40:41]
	v_or_b32_dpp v76, v29, v76 wave_shl:1 row_mask:0xf bank_mask:0xf bound_ctrl:1
	v_or3_b32 v17, v76, v89, v77
	v_or3_b32 v17, v17, v86, v87
	s_add_i32 s4, s34, 8
	s_cmpk_lt_u32 s4, 0x1ff
	s_cselect_b64 s[12:13], s[42:43], 0
	v_cmp_ne_u32_e64 s[30:31], 0, v17
	s_and_b64 s[30:31], s[30:31], s[12:13]
	v_cndmask_b32_e64 v17, 0, 1.0, s[30:31]
	v_pk_fma_f32 v[44:45], v[8:9], v[8:9], v[44:45] op_sel_hi:[0,1,1]
	v_pk_fma_f32 v[56:57], v[8:9], v[10:11], v[56:57] op_sel_hi:[1,0,1]
	v_fma_f32 v58, v9, v9, v58
	v_fma_f32 v59, v10, v10, v59
	v_add_f32_dpp v71, v17, v17 wave_shr:1 row_mask:0xf bank_mask:0xf bound_ctrl:1
	v_add_f32_e64 v70, v70, v42
	v_pk_fma_f32 v[44:45], v[40:41], v[40:41], v[44:45] op_sel_hi:[0,1,1]
	v_pk_fma_f32 v[56:57], v[40:41], v[42:43], v[56:57] op_sel_hi:[1,0,1]
	v_fma_f32 v58, v41, v41, v58
	v_fma_f32 v59, v42, v42, v59
	v_add_f32_dpp v71, v17, v71 wave_shl:1 row_mask:0xf bank_mask:0xf bound_ctrl:1
	v_pk_add_f32 v[84:85], v[64:65], v[38:39]
	v_pk_add_f32 v[90:91], v[6:7], v[84:85]
	v_pk_add_f32 v[6:7], v[78:79], v[44:45]
	v_pk_add_f32 v[64:65], v[20:21], v[6:7]
	v_pk_add_f32 v[20:21], v[96:97], v[56:57]
	v_pk_add_f32 v[78:79], v[46:47], v[20:21]
	v_pk_add_f32 v[96:97], v[102:103], v[58:59]
	v_pk_add_f32 v[46:47], v[50:51], v[96:97]
	v_pk_add_f32 v[50:51], v[106:107], v[70:71]
	v_pk_add_f32 v[100:101], v[52:53], v[50:51]
	v_mul_f32_e64 v112, v90, v22
	v_mul_f32_e64 v113, v91, v22
	v_mul_f32_e64 v114, v100, v22
	v_fma_f32 v17, v64, v22, v26
	v_mul_f32_e64 v29, v65, v22
	v_mul_f32_e64 v88, v78, v22
	v_fma_f32 v52, v46, v22, v26
	v_mul_f32_e64 v53, v79, v22
	v_fma_f32 v102, v47, v22, v26
	v_fma_f32 v17, -v112, v112, v17
	v_fma_f32 v29, -v112, v113, v29
	v_fma_f32 v88, -v112, v114, v88
	v_fma_f32 v52, -v113, v113, v52
	v_fma_f32 v53, -v113, v114, v53
	v_fma_f32 v102, -v114, v114, v102
	v_mul_f32_e64 v103, v53, v53
	v_mul_f32_e64 v106, v29, v102
	v_mul_f32_e64 v107, v88, v52
	v_mul_f32_e64 v124, v88, v88
	v_mul_f32_e64 v125, v17, v53
	v_mul_f32_e64 v126, v29, v29
	v_fma_f32 v103, v52, v102, -v103
	v_fma_f32 v106, v88, v53, -v106
	v_fma_f32 v107, v29, v53, -v107
	v_fma_f32 v124, v17, v102, -v124
	v_fma_f32 v125, v29, v88, -v125
	v_fma_f32 v126, v17, v52, -v126
	v_mul_f32_e64 v127, v17, v103
	v_fma_f32 v127, v29, v106, v127
	v_fma_f32 v127, v88, v107, v127
	v_rcp_f32_e32 v127, v127
	v_cmp_ne_u32_e64 vcc, s37, v25
	v_mul_f32_e64 v127, v127, v22
	v_cndmask_b32_e64 v127, 0, v127, s[30:31]
	v_cndmask_b32_e64 v17, 0, v18, vcc
	v_cndmask_b32_e64 v121, 0, v22, s[30:31]
	v_mul_f32_e64 v115, v103, v127
	v_mul_f32_e64 v116, v106, v127
	v_mul_f32_e64 v117, v107, v127
	v_mul_f32_e64 v118, v124, v127
	v_mul_f32_e64 v119, v125, v127
	v_mul_f32_e64 v120, v126, v127
	v_add_f32_e64 v122, v101, v17
	v_mov_b32_e32 v123, v25
	ds_write_b128 v23, v[112:115]
	ds_write_b128 v23, v[116:119] offset:1024
	ds_write_b128 v23, v[120:123] offset:2048
	v_mov_b32_dpp v46, v4 wave_shr:1 row_mask:0xf bank_mask:0xf bound_ctrl:1
	v_mov_b32_dpp v47, v5 wave_shr:1 row_mask:0xf bank_mask:0xf bound_ctrl:1
	v_mov_b32_dpp v78, v4 wave_shl:1 row_mask:0xf bank_mask:0xf bound_ctrl:1
	v_mov_b32_dpp v79, v5 wave_shl:1 row_mask:0xf bank_mask:0xf bound_ctrl:1
	v_pk_mul_f32 v[52:53], v[4:5], v[136:137] op_sel_hi:[1,0]
	v_pk_mul_f32 v[64:65], v[4:5], v[136:137] op_sel:[0,1]
	v_pk_mul_f32 v[100:101], v[4:5], v[138:139] op_sel_hi:[1,0]
	v_pk_add_f32 v[124:125], v[4:5], v[46:47]
	v_pk_fma_f32 v[52:53], v[46:47], v[8:9], v[52:53] op_sel_hi:[1,0,1]
	v_pk_fma_f32 v[64:65], v[46:47], v[8:9], v[64:65] op_sel:[0,1,0]
	v_pk_fma_f32 v[100:101], v[46:47], v[10:11], v[100:101] op_sel_hi:[1,0,1]
	v_pk_add_f32 v[124:125], v[124:125], v[78:79]
	v_pk_fma_f32 v[52:53], v[78:79], v[40:41], v[52:53] op_sel_hi:[1,0,1]
	v_pk_fma_f32 v[64:65], v[78:79], v[40:41], v[64:65] op_sel:[0,1,0]
	v_pk_fma_f32 v[100:101], v[78:79], v[42:43], v[100:101] op_sel_hi:[1,0,1]
	s_waitcnt lgkmcnt(0)
	s_barrier
	v_pk_add_f32 v[46:47], v[150:151], v[124:125]
	v_pk_add_f32 v[78:79], v[156:157], v[46:47]
	v_pk_add_f32 v[90:91], v[54:55], v[52:53]
	v_pk_add_f32 v[128:129], v[36:37], v[90:91]
	v_pk_add_f32 v[54:55], v[130:131], v[64:65]
	v_pk_add_f32 v[36:37], v[60:61], v[54:55]
	v_pk_add_f32 v[102:103], v[134:135], v[100:101]
	v_pk_add_f32 v[60:61], v[152:153], v[102:103]
	v_pk_fma_f32 v[128:129], v[112:113], v[78:79], v[128:129] op_sel_hi:[0,1,1] neg_lo:[1,0,0] neg_hi:[1,0,0]
	v_pk_fma_f32 v[36:37], v[112:113], v[78:79], v[36:37] op_sel:[1,0,0] neg_lo:[1,0,0] neg_hi:[1,0,0]
	v_pk_fma_f32 v[60:61], v[114:115], v[78:79], v[60:61] op_sel_hi:[0,1,1] neg_lo:[1,0,0] neg_hi:[1,0,0]
	v_pk_mul_f32 v[106:107], v[114:115], v[128:129] op_sel:[1,0]
	v_pk_mul_f32 v[126:127], v[116:117], v[128:129] op_sel_hi:[0,1]
	v_pk_mul_f32 v[130:131], v[116:117], v[128:129] op_sel:[1,0]
	v_pk_fma_f32 v[106:107], v[116:117], v[36:37], v[106:107] op_sel_hi:[0,1,1]
	v_pk_fma_f32 v[126:127], v[118:119], v[36:37], v[126:127] op_sel_hi:[0,1,1]
	v_pk_fma_f32 v[130:131], v[118:119], v[36:37], v[130:131] op_sel:[1,0,0]
	v_pk_fma_f32 v[106:107], v[116:117], v[60:61], v[106:107] op_sel:[1,0,0]
	v_pk_fma_f32 v[126:127], v[118:119], v[60:61], v[126:127] op_sel:[1,0,0]
	v_pk_fma_f32 v[130:131], v[120:121], v[60:61], v[130:131] op_sel_hi:[0,1,1]
	v_pk_mul_f32 v[132:133], v[112:113], v[106:107] op_sel_hi:[0,1]
	v_pk_fma_f32 v[132:133], v[112:113], v[126:127], v[132:133] op_sel:[1,0,0]
	v_pk_fma_f32 v[132:133], v[114:115], v[130:131], v[132:133] op_sel_hi:[0,1,1]
	v_pk_fma_f32 v[132:133], v[120:121], v[78:79], v[132:133] op_sel:[1,0,0] neg_lo:[0,0,1] neg_hi:[0,0,1]
	v_cmp_eq_u32_e64 s[10:11], 6, v123
	v_cmp_eq_u32_e64 s[14:15], 7, v123
	v_pk_add_f32 v[36:37], v[68:69], v[106:107]
	v_pk_add_f32 v[60:61], v[94:95], v[36:37]
	v_pk_add_f32 v[68:69], v[104:105], v[126:127]
	v_pk_add_f32 v[78:79], v[98:99], v[68:69]
	v_pk_add_f32 v[104:105], v[108:109], v[130:131]
	v_pk_add_f32 v[94:95], v[110:111], v[104:105]
	v_pk_add_f32 v[98:99], v[62:63], v[132:133]
	v_pk_add_f32 v[108:109], v[92:93], v[98:99]
	v_pk_fma_f32 v[92:93], v[12:13], v[60:61], v[108:109] op_sel_hi:[0,1,1]
	v_pk_fma_f32 v[128:129], v[80:81], v[60:61], v[108:109] op_sel_hi:[0,1,1]
	v_pk_fma_f32 v[92:93], v[12:13], v[78:79], v[92:93] op_sel:[1,0,0]
	v_pk_fma_f32 v[128:129], v[80:81], v[78:79], v[128:129] op_sel:[1,0,0]
	v_pk_fma_f32 v[92:93], v[14:15], v[94:95], v[92:93] op_sel_hi:[0,1,1]
	v_pk_fma_f32 v[128:129], v[82:83], v[94:95], v[128:129] op_sel_hi:[0,1,1]
	v_pk_fma_f32 v[108:109], v[140:141], v[60:61], v[108:109] op_sel_hi:[0,1,1]
	v_pk_fma_f32 v[108:109], v[140:141], v[78:79], v[108:109] op_sel:[1,0,0]
	v_pk_fma_f32 v[108:109], v[142:143], v[94:95], v[108:109] op_sel_hi:[0,1,1]
	v_cndmask_b32_e64 v62, 0, v18, s[10:11]
	v_cndmask_b32_e64 v63, 0, v18, s[14:15]
	v_add_f32_dpp v108, v92, v108 wave_shl:1 row_mask:0xf bank_mask:0xf bound_ctrl:1
	v_add_f32_dpp v109, v93, v109 wave_shl:1 row_mask:0xf bank_mask:0xf bound_ctrl:1
	s_add_i32 s4, s34, 8
	s_cmpk_lt_i32 s4, 0x201
	s_cselect_b64 s[12:13], s[0:1], 0
	v_add_f32_dpp v108, v128, v108 wave_shr:1 row_mask:0xf bank_mask:0xf bound_ctrl:1
	v_add_f32_dpp v109, v129, v109 wave_shr:1 row_mask:0xf bank_mask:0xf bound_ctrl:1
	v_pk_fma_f32 v[108:109], v[48:49], v[122:123], v[108:109] op_sel_hi:[1,0,1] neg_lo:[0,0,1] neg_hi:[0,0,1]
	v_pk_add_f32 v[108:109], v[108:109], v[62:63] neg_lo:[0,1] neg_hi:[0,1]
	v_pk_mul_f32 v[110:111], v[108:109], v[108:109]
	v_add_f32_e32 v110, v110, v111
	v_cndmask_b32_e64 v111, 0, v110, s[12:13]
	v_add_f32_e32 v1, v1, v111
	s_waitcnt vmcnt(0)
	v_mov_b32_dpp v12, v160 wave_shr:1 row_mask:0xf bank_mask:0xf bound_ctrl:1
	v_mov_b32_dpp v13, v161 wave_shr:1 row_mask:0xf bank_mask:0xf bound_ctrl:1
	v_mov_b32_dpp v14, v162 wave_shr:1 row_mask:0xf bank_mask:0xf bound_ctrl:1
	v_mov_b32_dpp v60, v160 wave_shl:1 row_mask:0xf bank_mask:0xf bound_ctrl:1
	v_mov_b32_dpp v61, v161 wave_shl:1 row_mask:0xf bank_mask:0xf bound_ctrl:1
	v_mov_b32_dpp v62, v162 wave_shl:1 row_mask:0xf bank_mask:0xf bound_ctrl:1
	s_add_i32 s4, s34, 12
	s_cmpk_lt_u32 s4, 0x201
	s_cselect_b64 s[12:13], s[40:41], 0
	v_cmp_eq_u32_e64 s[14:15], s37, v16
	s_and_b64 s[14:15], s[14:15], s[12:13]
	v_cndmask_b32_e64 v17, 0, 1, s[14:15]
	v_pk_add_f32 v[48:49], v[160:161], v[12:13]
	v_pk_mul_f32 v[78:79], v[160:161], v[160:161] op_sel_hi:[0,1]
	v_or_b32_dpp v25, v17, v17 wave_shr:1 row_mask:0xf bank_mask:0xf bound_ctrl:1
	v_pk_mul_f32 v[80:81], v[160:161], v[162:163] op_sel_hi:[1,0]
	v_or_b32_dpp v25, v17, v25 wave_shl:1 row_mask:0xf bank_mask:0xf bound_ctrl:1
	v_mul_f32_e64 v82, v161, v161
	v_mul_f32_e64 v83, v162, v162
	v_or_b32_dpp v29, v25, v25 wave_shr:1 row_mask:0xf bank_mask:0xf bound_ctrl:1
	v_add_f32_e64 v92, v162, v14
	v_pk_add_f32 v[48:49], v[48:49], v[60:61]
	v_or_b32_dpp v29, v25, v29 wave_shl:1 row_mask:0xf bank_mask:0xf bound_ctrl:1
	v_or3_b32 v17, v29, v76, v89
	v_or3_b32 v17, v17, v77, v86
	s_add_i32 s4, s34, 9
	s_cmpk_lt_u32 s4, 0x1ff
	s_cselect_b64 s[12:13], s[42:43], 0
	v_cmp_ne_u32_e64 s[30:31], 0, v17
	s_and_b64 s[30:31], s[30:31], s[12:13]
	v_cndmask_b32_e64 v17, 0, 1.0, s[30:31]
	v_pk_fma_f32 v[78:79], v[12:13], v[12:13], v[78:79] op_sel_hi:[0,1,1]
	v_pk_fma_f32 v[80:81], v[12:13], v[14:15], v[80:81] op_sel_hi:[1,0,1]
	v_fma_f32 v82, v13, v13, v82
	v_fma_f32 v83, v14, v14, v83
	v_add_f32_dpp v93, v17, v17 wave_shr:1 row_mask:0xf bank_mask:0xf bound_ctrl:1
	v_add_f32_e64 v92, v92, v62
	v_pk_fma_f32 v[78:79], v[60:61], v[60:61], v[78:79] op_sel_hi:[0,1,1]
	v_pk_fma_f32 v[80:81], v[60:61], v[62:63], v[80:81] op_sel_hi:[1,0,1]
	v_fma_f32 v82, v61, v61, v82
	v_fma_f32 v83, v62, v62, v83
	v_add_f32_dpp v93, v17, v93 wave_shl:1 row_mask:0xf bank_mask:0xf bound_ctrl:1
	v_pk_add_f32 v[94:95], v[84:85], v[48:49]
	v_pk_add_f32 v[84:85], v[6:7], v[78:79]
	v_pk_add_f32 v[6:7], v[20:21], v[80:81]
	v_pk_add_f32 v[20:21], v[96:97], v[82:83]
	v_pk_add_f32 v[96:97], v[50:51], v[92:93]
	v_mul_f32_e64 v108, v94, v22
	v_mul_f32_e64 v109, v95, v22
	v_mul_f32_e64 v110, v96, v22
	v_fma_f32 v17, v84, v22, v26
	v_mul_f32_e64 v25, v85, v22
	v_mul_f32_e64 v87, v6, v22
	v_fma_f32 v88, v20, v22, v26
	v_mul_f32_e64 v50, v7, v22
	v_fma_f32 v51, v21, v22, v26
	v_fma_f32 v17, -v108, v108, v17
	v_fma_f32 v25, -v108, v109, v25
	v_fma_f32 v87, -v108, v110, v87
	v_fma_f32 v88, -v109, v109, v88
	v_fma_f32 v50, -v109, v110, v50
	v_fma_f32 v51, -v110, v110, v51
	v_mul_f32_e64 v120, v50, v50
	v_mul_f32_e64 v121, v25, v51
	v_mul_f32_e64 v122, v87, v88
	v_mul_f32_e64 v123, v87, v87
	v_mul_f32_e64 v128, v17, v50
	v_mul_f32_e64 v129, v25, v25
	v_fma_f32 v120, v88, v51, -v120
	v_fma_f32 v121, v87, v50, -v121
	v_fma_f32 v122, v25, v50, -v122
	v_fma_f32 v123, v17, v51, -v123
	v_fma_f32 v128, v25, v87, -v128
	v_fma_f32 v129, v17, v88, -v129
	v_mul_f32_e64 v134, v17, v120
	v_fma_f32 v134, v25, v121, v134
	v_fma_f32 v134, v87, v122, v134
	v_rcp_f32_e32 v134, v134
	v_cmp_ne_u32_e64 vcc, s37, v24
	v_mul_f32_e64 v134, v134, v22
	v_cndmask_b32_e64 v134, 0, v134, s[30:31]
	v_cndmask_b32_e64 v17, 0, v18, vcc
	v_cndmask_b32_e64 v117, 0, v22, s[30:31]
	v_mul_f32_e64 v111, v120, v134
	v_mul_f32_e64 v112, v121, v134
	v_mul_f32_e64 v113, v122, v134
	v_mul_f32_e64 v114, v123, v134
	v_mul_f32_e64 v115, v128, v134
	v_mul_f32_e64 v116, v129, v134
	v_add_f32_e64 v118, v97, v17
	v_mov_b32_e32 v119, v24
	ds_write_b128 v23, v[108:111] offset:3072
	ds_write_b128 v23, v[112:115] offset:4096
	ds_write_b128 v23, v[116:119] offset:5120
	v_mov_b32_dpp v20, v66 wave_shr:1 row_mask:0xf bank_mask:0xf bound_ctrl:1
	v_mov_b32_dpp v21, v67 wave_shr:1 row_mask:0xf bank_mask:0xf bound_ctrl:1
	v_mov_b32_dpp v24, v66 wave_shl:1 row_mask:0xf bank_mask:0xf bound_ctrl:1
	v_mov_b32_dpp v25, v67 wave_shl:1 row_mask:0xf bank_mask:0xf bound_ctrl:1
	v_pk_mul_f32 v[6:7], v[66:67], v[160:161] op_sel_hi:[1,0]
	v_pk_mul_f32 v[50:51], v[66:67], v[160:161] op_sel:[0,1]
	v_pk_mul_f32 v[86:87], v[66:67], v[162:163] op_sel_hi:[1,0]
	v_pk_add_f32 v[94:95], v[66:67], v[20:21]
	v_pk_fma_f32 v[6:7], v[20:21], v[12:13], v[6:7] op_sel_hi:[1,0,1]
	v_pk_fma_f32 v[50:51], v[20:21], v[12:13], v[50:51] op_sel:[0,1,0]
	v_pk_fma_f32 v[86:87], v[20:21], v[14:15], v[86:87] op_sel_hi:[1,0,1]
	v_pk_add_f32 v[94:95], v[94:95], v[24:25]
	v_pk_fma_f32 v[6:7], v[24:25], v[60:61], v[6:7] op_sel_hi:[1,0,1]
	v_pk_fma_f32 v[50:51], v[24:25], v[60:61], v[50:51] op_sel:[0,1,0]
	v_pk_fma_f32 v[86:87], v[24:25], v[62:63], v[86:87] op_sel_hi:[1,0,1]
	s_waitcnt lgkmcnt(0)
	s_barrier
	v_pk_add_f32 v[20:21], v[46:47], v[94:95]
	v_pk_add_f32 v[46:47], v[90:91], v[6:7]
	v_pk_add_f32 v[90:91], v[54:55], v[50:51]
	v_pk_add_f32 v[54:55], v[102:103], v[86:87]
	v_pk_fma_f32 v[46:47], v[108:109], v[20:21], v[46:47] op_sel_hi:[0,1,1] neg_lo:[1,0,0] neg_hi:[1,0,0]
	v_pk_fma_f32 v[90:91], v[108:109], v[20:21], v[90:91] op_sel:[1,0,0] neg_lo:[1,0,0] neg_hi:[1,0,0]
	v_pk_fma_f32 v[54:55], v[110:111], v[20:21], v[54:55] op_sel_hi:[0,1,1] neg_lo:[1,0,0] neg_hi:[1,0,0]
	v_pk_mul_f32 v[24:25], v[110:111], v[46:47] op_sel:[1,0]
	v_pk_mul_f32 v[84:85], v[112:113], v[46:47] op_sel_hi:[0,1]
	v_pk_mul_f32 v[96:97], v[112:113], v[46:47] op_sel:[1,0]
	v_pk_fma_f32 v[24:25], v[112:113], v[90:91], v[24:25] op_sel_hi:[0,1,1]
	v_pk_fma_f32 v[84:85], v[114:115], v[90:91], v[84:85] op_sel_hi:[0,1,1]
	v_pk_fma_f32 v[96:97], v[114:115], v[90:91], v[96:97] op_sel:[1,0,0]
	v_pk_fma_f32 v[24:25], v[112:113], v[54:55], v[24:25] op_sel:[1,0,0]
	v_pk_fma_f32 v[84:85], v[114:115], v[54:55], v[84:85] op_sel:[1,0,0]
	v_pk_fma_f32 v[96:97], v[116:117], v[54:55], v[96:97] op_sel_hi:[0,1,1]
	v_pk_mul_f32 v[102:103], v[108:109], v[24:25] op_sel_hi:[0,1]
	v_pk_fma_f32 v[102:103], v[108:109], v[84:85], v[102:103] op_sel:[1,0,0]
	v_pk_fma_f32 v[102:103], v[110:111], v[96:97], v[102:103] op_sel_hi:[0,1,1]
	v_pk_fma_f32 v[102:103], v[116:117], v[20:21], v[102:103] op_sel:[1,0,0] neg_lo:[0,0,1] neg_hi:[0,0,1]
	v_cmp_eq_u32_e64 s[10:11], 6, v119
	v_cmp_eq_u32_e64 s[14:15], 7, v119
	v_pk_add_f32 v[20:21], v[36:37], v[24:25]
	v_pk_add_f32 v[36:37], v[68:69], v[84:85]
	v_pk_add_f32 v[46:47], v[104:105], v[96:97]
	v_pk_add_f32 v[54:55], v[98:99], v[102:103]
	v_pk_fma_f32 v[90:91], v[32:33], v[20:21], v[54:55] op_sel_hi:[0,1,1]
	v_pk_fma_f32 v[98:99], v[72:73], v[20:21], v[54:55] op_sel_hi:[0,1,1]
	v_pk_fma_f32 v[90:91], v[32:33], v[36:37], v[90:91] op_sel:[1,0,0]
	v_pk_fma_f32 v[98:99], v[72:73], v[36:37], v[98:99] op_sel:[1,0,0]
	v_pk_fma_f32 v[90:91], v[34:35], v[46:47], v[90:91] op_sel_hi:[0,1,1]
	v_pk_fma_f32 v[98:99], v[74:75], v[46:47], v[98:99] op_sel_hi:[0,1,1]
	v_pk_fma_f32 v[54:55], v[144:145], v[20:21], v[54:55] op_sel_hi:[0,1,1]
	v_pk_fma_f32 v[54:55], v[144:145], v[36:37], v[54:55] op_sel:[1,0,0]
	v_pk_fma_f32 v[54:55], v[146:147], v[46:47], v[54:55] op_sel_hi:[0,1,1]
	v_cndmask_b32_e64 v68, 0, v18, s[10:11]
	v_cndmask_b32_e64 v69, 0, v18, s[14:15]
	v_add_f32_dpp v54, v90, v54 wave_shl:1 row_mask:0xf bank_mask:0xf bound_ctrl:1
	v_add_f32_dpp v55, v91, v55 wave_shl:1 row_mask:0xf bank_mask:0xf bound_ctrl:1
	s_add_i32 s4, s34, 9
	s_cmpk_lt_i32 s4, 0x201
	s_cselect_b64 s[12:13], s[0:1], 0
	v_add_f32_dpp v54, v98, v54 wave_shr:1 row_mask:0xf bank_mask:0xf bound_ctrl:1
	v_add_f32_dpp v55, v99, v55 wave_shr:1 row_mask:0xf bank_mask:0xf bound_ctrl:1
	v_pk_fma_f32 v[54:55], v[30:31], v[118:119], v[54:55] op_sel_hi:[1,0,1] neg_lo:[0,0,1] neg_hi:[0,0,1]
	v_pk_add_f32 v[54:55], v[54:55], v[68:69] neg_lo:[0,1] neg_hi:[0,1]
	v_pk_mul_f32 v[104:105], v[54:55], v[54:55]
	v_add_f32_e32 v104, v104, v105
	v_cndmask_b32_e64 v105, 0, v104, s[12:13]
	v_add_f32_e32 v1, v1, v105
	v_mov_b32_e32 v0, v1
	s_branch .LBB0_29
